# v78 plus nt on read-once / last-use activation row loads: P1 input rows, P4 epilogue residual input rows, P12 residual rows
# speedup vs baseline: 1.0127x; 1.0051x over previous
; __device__ __forceinline__ unsigned cvt_pk_bf16(float lo, float hi) { unsigned r; asm volatile("v_cvt_pk_bf16_f32 %0, %1, %2" : "=v"(r) : "v"(lo), "v"(hi)); return r; }
; #define GAS __attribute__((address_space(1)))
; __device__ __forceinline__ void norm_mod_rows(Frame& F, const float* xin, const float* g, const float* shift, const float* scale, bf16* XN) {
;     ...
;         for (int r = 0; r < 8; ++r) {
;             const GAS f32x4* xr = (const GAS f32x4*)(xin + (size_t)(row0 + r) * D) + lane;
;             f32x4 v[4]; float s = 0.f;
; #pragma unroll
;             for (int j = 0; j < 4; ++j) { v[j] = xr[64 * j]; s += (v[j].x * v[j].x + v[j].y * v[j].y) + (v[j].z * v[j].z + v[j].w * v[j].w); }
;             const float rstd = rsqrtf(wave_sum(s) * (1.f / D) + RMS_EPS);
;             GAS unsigned long long* o8 = (GAS unsigned long long*)(XN + (size_t)(row0 + r) * D) + lane;
; #pragma unroll
;             for (int j = 0; j < 4; ++j) { const f32x4 y = v[j] * rstd * gs[j] + sh[j];
;                 o8[64 * j] = (unsigned long long)pg8::cvt_pk_bf16(y.x, y.y) | ((unsigned long long)pg8::cvt_pk_bf16(y.z, y.w) << 32); }
.LBB0_128:
	global_load_dwordx4 v[58:61], v[32:33], off offset:-3072 nt
	global_load_dwordx4 v[62:65], v[32:33], off offset:-2048 nt
	global_load_dwordx4 v[66:69], v[32:33], off nt
	global_load_dwordx4 v[70:73], v[32:33], off offset:-1024 nt
	v_lshl_add_u64 v[74:75], v[30:31], 0, s[10:11]
	v_add_co_u32_e32 v74, vcc, s18, v74
	s_ashr_i32 s13, s12, 31
	s_nop 0
	v_addc_co_u32_e32 v75, vcc, 0, v75, vcc
	s_lshl_b64 s[20:21], s[12:13], 12
	v_lshl_add_u64 v[76:77], v[18:19], 0, s[20:21]
	s_lshl_b64 s[20:21], s[12:13], 11
	s_add_i32 s12, s12, 2
	s_add_u32 s10, s10, 0x1000
	s_addc_u32 s11, s11, 0
	v_lshl_add_u64 v[32:33], v[32:33], 0, s[8:9]
	s_cmpk_eq_i32 s10, 0x4000
	s_waitcnt vmcnt(3)
	v_pk_mul_f32 v[78:79], v[60:61], v[60:61]
	v_pk_mul_f32 v[80:81], v[58:59], v[58:59]
	s_waitcnt vmcnt(2)
	v_pk_mul_f32 v[82:83], v[64:65], v[64:65]
	v_pk_mul_f32 v[84:85], v[62:63], v[62:63]
	v_pk_mov_b32 v[90:91], v[80:81], v[78:79] op_sel:[1,0]
	v_mov_b32_e32 v81, v79
	v_pk_mov_b32 v[78:79], v[84:85], v[82:83] op_sel:[1,0]
	v_mov_b32_e32 v85, v83
	s_waitcnt vmcnt(1)
	v_mul_f32_e32 v89, v66, v66
	s_waitcnt vmcnt(0)
	v_mul_f32_e32 v86, v71, v71
	v_mul_f32_e32 v88, v73, v73
	v_pk_add_f32 v[80:81], v[90:91], v[80:81]
	v_pk_add_f32 v[78:79], v[78:79], v[84:85]
	v_mul_f32_e32 v92, v67, v67
	v_mul_f32_e32 v93, v68, v68
	v_mul_f32_e32 v94, v69, v69
	v_pk_fma_f32 v[82:83], v[70:71], v[70:71], v[86:87] op_sel_hi:[1,1,0]
	v_pk_fma_f32 v[86:87], v[72:73], v[72:73], v[88:89] op_sel_hi:[1,1,0]
	v_pk_add_f32 v[80:81], v[80:81], v[80:81] op_sel:[0,1] op_sel_hi:[1,0]
	v_pk_add_f32 v[78:79], v[78:79], v[78:79] op_sel:[0,1] op_sel_hi:[1,0]
	v_mov_b32_e32 v83, v93
	v_mov_b32_e32 v87, v94
	v_mov_b32_e32 v81, v89
	v_mov_b32_e32 v79, v92
	v_pk_add_f32 v[82:83], v[82:83], v[86:87]
	v_pk_add_f32 v[78:79], v[80:81], v[78:79]
	s_nop 0
	v_pk_add_f32 v[78:79], v[78:79], v[82:83]
	s_nop 0
	v_add_f32_e32 v78, v78, v79
	ds_bpermute_b32 v79, v50, v78
	s_waitcnt lgkmcnt(0)
	v_add_f32_e32 v78, v78, v79
	ds_bpermute_b32 v79, v51, v78
	s_waitcnt lgkmcnt(0)
	v_add_f32_e32 v78, v78, v79
	ds_bpermute_b32 v79, v52, v78
	s_waitcnt lgkmcnt(0)
	v_add_f32_e32 v78, v78, v79
	ds_bpermute_b32 v79, v53, v78
	s_waitcnt lgkmcnt(0)
	v_add_f32_e32 v78, v78, v79
	ds_bpermute_b32 v79, v54, v78
	s_waitcnt lgkmcnt(0)
	v_add_f32_e32 v78, v78, v79
	ds_bpermute_b32 v79, v55, v78
	s_waitcnt lgkmcnt(0)
	v_add_f32_e32 v78, v78, v79
	v_fmamk_f32 v78, v78, 0x3a800000, v57
	v_mul_f32_e32 v79, 0x4b800000, v78
	v_cmp_gt_f32_e32 vcc, s17, v78
	s_nop 1
	v_cndmask_b32_e32 v78, v78, v79, vcc
	v_rsq_f32_e32 v78, v78
	s_nop 0
	v_mul_f32_e32 v79, 0x45800000, v78
	v_cndmask_b32_e32 v78, v78, v79, vcc
	v_pk_mul_f32 v[58:59], v[58:59], v[78:79] op_sel_hi:[1,0]
	v_pk_mul_f32 v[60:61], v[60:61], v[78:79] op_sel_hi:[1,0]
	v_pk_fma_f32 v[58:59], v[36:37], v[58:59], v[0:1]
	v_pk_mul_f32 v[62:63], v[62:63], v[78:79] op_sel_hi:[1,0]
	v_pk_mul_f32 v[64:65], v[64:65], v[78:79] op_sel_hi:[1,0]
	v_pk_fma_f32 v[60:61], v[34:35], v[60:61], v[2:3]
	v_cvt_pk_bf16_f32 v58, v58, v59
	v_pk_mul_f32 v[70:71], v[70:71], v[78:79] op_sel_hi:[1,0]
	v_cvt_pk_bf16_f32 v59, v60, v61
	v_pk_mul_f32 v[72:73], v[72:73], v[78:79] op_sel_hi:[1,0]
	v_pk_fma_f32 v[64:65], v[38:39], v[64:65], v[6:7]
	v_pk_fma_f32 v[62:63], v[40:41], v[62:63], v[4:5]
	global_store_dwordx2 v[74:75], v[58:59], off
	v_cvt_pk_bf16_f32 v58, v62, v63
	v_cvt_pk_bf16_f32 v59, v64, v65
	v_pk_mul_f32 v[66:67], v[66:67], v[78:79] op_sel_hi:[1,0]
	v_pk_mul_f32 v[68:69], v[68:69], v[78:79] op_sel_hi:[1,0]
	v_pk_fma_f32 v[72:73], v[42:43], v[72:73], v[10:11]
	v_pk_fma_f32 v[70:71], v[44:45], v[70:71], v[8:9]
	global_store_dwordx2 v[74:75], v[58:59], off offset:512
	v_cvt_pk_bf16_f32 v58, v70, v71
	v_cvt_pk_bf16_f32 v59, v72, v73
	v_pk_fma_f32 v[68:69], v[46:47], v[68:69], v[14:15]
	v_pk_fma_f32 v[66:67], v[48:49], v[66:67], v[12:13]
	global_store_dwordx2 v[74:75], v[58:59], off offset:1024
	v_cvt_pk_bf16_f32 v58, v66, v67
	v_cvt_pk_bf16_f32 v59, v68, v69
	global_store_dwordx2 v[74:75], v[58:59], off offset:1536
	global_load_dwordx4 v[58:61], v[76:77], off nt
	s_nop 0
	global_load_dwordx4 v[62:65], v[76:77], off offset:1024 nt
	global_load_dwordx4 v[66:69], v[76:77], off offset:2048 nt
	global_load_dwordx4 v[70:73], v[76:77], off offset:3072 nt
	v_lshl_add_u64 v[74:75], v[20:21], 0, s[20:21]
	s_waitcnt vmcnt(3)
; __device__ __forceinline__ unsigned cvt_pk_bf16(float lo, float hi) { unsigned r; asm volatile("v_cvt_pk_bf16_f32 %0, %1, %2" : "=v"(r) : "v"(lo), "v"(hi)); return r; }
; #define GAS __attribute__((address_space(1)))
; __device__ __forceinline__ void norm_mod_rows(Frame& F, const float* xin, const float* g, const float* shift, const float* scale, bf16* XN) {
;     ...
;         for (int r = 0; r < 8; ++r) {
;             const GAS f32x4* xr = (const GAS f32x4*)(xin + (size_t)(row0 + r) * D) + lane;
;             f32x4 v[4]; float s = 0.f;
; #pragma unroll
;             for (int j = 0; j < 4; ++j) { v[j] = xr[64 * j]; s += (v[j].x * v[j].x + v[j].y * v[j].y) + (v[j].z * v[j].z + v[j].w * v[j].w); }
;             const float rstd = rsqrtf(wave_sum(s) * (1.f / D) + RMS_EPS);
;             GAS unsigned long long* o8 = (GAS unsigned long long*)(XN + (size_t)(row0 + r) * D) + lane;
; #pragma unroll
;             for (int j = 0; j < 4; ++j) { const f32x4 y = v[j] * rstd * gs[j] + sh[j];
;                 o8[64 * j] = (unsigned long long)pg8::cvt_pk_bf16(y.x, y.y) | ((unsigned long long)pg8::cvt_pk_bf16(y.z, y.w) << 32); }
;         }
	v_pk_mul_f32 v[76:77], v[60:61], v[60:61]
	v_pk_mul_f32 v[78:79], v[58:59], v[58:59]
	s_waitcnt vmcnt(2)
	v_pk_mul_f32 v[80:81], v[64:65], v[64:65]
	v_pk_mul_f32 v[82:83], v[62:63], v[62:63]
	v_pk_mov_b32 v[88:89], v[78:79], v[76:77] op_sel:[1,0]
	v_mov_b32_e32 v79, v77
	v_pk_mov_b32 v[76:77], v[82:83], v[80:81] op_sel:[1,0]
	v_mov_b32_e32 v83, v81
	s_waitcnt vmcnt(0)
	v_mul_f32_e32 v87, v70, v70
	v_mul_f32_e32 v84, v67, v67
	v_mul_f32_e32 v86, v69, v69
	v_pk_add_f32 v[78:79], v[88:89], v[78:79]
	v_pk_add_f32 v[76:77], v[76:77], v[82:83]
	v_mul_f32_e32 v90, v71, v71
	v_mul_f32_e32 v91, v72, v72
	v_mul_f32_e32 v92, v73, v73
	v_pk_fma_f32 v[80:81], v[66:67], v[66:67], v[84:85] op_sel_hi:[1,1,0]
	v_pk_fma_f32 v[84:85], v[68:69], v[68:69], v[86:87] op_sel_hi:[1,1,0]
	v_pk_add_f32 v[78:79], v[78:79], v[78:79] op_sel:[0,1] op_sel_hi:[1,0]
	v_pk_add_f32 v[76:77], v[76:77], v[76:77] op_sel:[0,1] op_sel_hi:[1,0]
	v_mov_b32_e32 v81, v91
	v_mov_b32_e32 v85, v92
	v_mov_b32_e32 v79, v87
	v_mov_b32_e32 v77, v90
	v_pk_add_f32 v[80:81], v[80:81], v[84:85]
	v_pk_add_f32 v[76:77], v[78:79], v[76:77]
	s_nop 0
	v_pk_add_f32 v[76:77], v[76:77], v[80:81]
	s_nop 0
	v_add_f32_e32 v76, v76, v77
	ds_bpermute_b32 v77, v50, v76
	s_waitcnt lgkmcnt(0)
	v_add_f32_e32 v76, v76, v77
	ds_bpermute_b32 v77, v51, v76
	s_waitcnt lgkmcnt(0)
	v_add_f32_e32 v76, v76, v77
	ds_bpermute_b32 v77, v52, v76
	s_waitcnt lgkmcnt(0)
	v_add_f32_e32 v76, v76, v77
	ds_bpermute_b32 v77, v53, v76
	s_waitcnt lgkmcnt(0)
	v_add_f32_e32 v76, v76, v77
	ds_bpermute_b32 v77, v54, v76
	s_waitcnt lgkmcnt(0)
	v_add_f32_e32 v76, v76, v77
	ds_bpermute_b32 v77, v55, v76
	s_waitcnt lgkmcnt(0)
	v_add_f32_e32 v76, v76, v77
	v_fmamk_f32 v76, v76, 0x3a800000, v57
	v_mul_f32_e32 v77, 0x4b800000, v76
	v_cmp_gt_f32_e32 vcc, s17, v76
	s_nop 1
	v_cndmask_b32_e32 v76, v76, v77, vcc
	v_rsq_f32_e32 v76, v76
	s_nop 0
	v_mul_f32_e32 v77, 0x45800000, v76
	v_cndmask_b32_e32 v76, v76, v77, vcc
	v_pk_mul_f32 v[58:59], v[58:59], v[76:77] op_sel_hi:[1,0]
	v_pk_mul_f32 v[60:61], v[60:61], v[76:77] op_sel_hi:[1,0]
	v_pk_fma_f32 v[58:59], v[36:37], v[58:59], v[0:1]
	v_pk_mul_f32 v[62:63], v[62:63], v[76:77] op_sel_hi:[1,0]
	v_pk_mul_f32 v[64:65], v[64:65], v[76:77] op_sel_hi:[1,0]
	v_pk_fma_f32 v[60:61], v[34:35], v[60:61], v[2:3]
	v_cvt_pk_bf16_f32 v58, v58, v59
	v_pk_mul_f32 v[66:67], v[66:67], v[76:77] op_sel_hi:[1,0]
	v_cvt_pk_bf16_f32 v59, v60, v61
	v_pk_mul_f32 v[68:69], v[68:69], v[76:77] op_sel_hi:[1,0]
	v_pk_fma_f32 v[64:65], v[38:39], v[64:65], v[6:7]
	v_pk_fma_f32 v[62:63], v[40:41], v[62:63], v[4:5]
	global_store_dwordx2 v[74:75], v[58:59], off
	v_cvt_pk_bf16_f32 v58, v62, v63
	v_cvt_pk_bf16_f32 v59, v64, v65
	v_pk_mul_f32 v[70:71], v[70:71], v[76:77] op_sel_hi:[1,0]
	v_pk_mul_f32 v[72:73], v[72:73], v[76:77] op_sel_hi:[1,0]
	v_pk_fma_f32 v[68:69], v[42:43], v[68:69], v[10:11]
	v_pk_fma_f32 v[66:67], v[44:45], v[66:67], v[8:9]
	global_store_dwordx2 v[74:75], v[58:59], off offset:512
	v_cvt_pk_bf16_f32 v58, v66, v67
	v_cvt_pk_bf16_f32 v59, v68, v69
	v_pk_fma_f32 v[72:73], v[46:47], v[72:73], v[14:15]
	v_pk_fma_f32 v[70:71], v[48:49], v[70:71], v[12:13]
	global_store_dwordx2 v[74:75], v[58:59], off offset:1024
	v_cvt_pk_bf16_f32 v58, v70, v71
	v_cvt_pk_bf16_f32 v59, v72, v73
	global_store_dwordx2 v[74:75], v[58:59], off offset:1536
	s_cbranch_scc0 .LBB0_128
	s_add_i32 s3, s3, s14
	s_add_i32 s15, s15, s16
	s_add_i32 s0, s0, s16
	s_cmpk_gt_i32 s3, 0x7ff
	s_cbranch_scc0 .LBB0_127

; __device__ __forceinline__ u32x4 pk8(const f32x4 a, const f32x4 b) { u32x4 q; q.x = cvt_pk_bf16(a[0], a[1]); q.y = cvt_pk_bf16(a[2], a[3]); q.z = cvt_pk_bf16(b[0], b[1]); q.w = cvt_pk_bf16(b[2], b[3]); return q; }
;     __device__ __forceinline__ void fused(f32x4 (&acc)[2][2][4][2], const Unit& u, int wr, int wc, int fr, int fq, PG8_LAS unsigned char* lds, int wid, int lane) const {
;     ...
;         const int row0 = u.orow + wr * 64 + fr, col0 = u.ocol * BM + wc * 32 + 8 * fq; const size_t boff = (size_t)(u.orow / rows_per_batch) * gld + col0;
;         { f32x4 gv[2][2];
; #pragma unroll
;           for (int bj = 0; bj < 2; ++bj)
; #pragma unroll
;               for (int n = 0; n < 2; ++n) gv[bj][n] = *(const f32x4*)(gate + boff + bj * HALF + n * 4) * asc;
;           bf16_t* op = out + (size_t)row0 * ldc + col0;
;           if constexpr (XF32) {
;               const float* xp = (const float*)xin + (size_t)row0 * ldc + col0; f32x4 xv[4][2][2];
; #pragma unroll
;               for (int ai = 0; ai < 2; ++ai) {
; #pragma unroll
;                   for (int m = 0; m < 4; ++m)
; #pragma unroll
;                       for (int bj = 0; bj < 2; ++bj)
; #pragma unroll
;                           for (int n = 0; n < 2; ++n) xv[m][bj][n] = *(const f32x4*)(xp + (size_t)(ai * HALF + m * 16) * ldc + bj * HALF + n * 4);
; #pragma unroll
;                   for (int m = 0; m < 4; ++m)
; #pragma unroll
;                       for (int bj = 0; bj < 2; ++bj) { acc[ai][bj][m][0] = xv[m][bj][0] + gv[bj][0] * acc[ai][bj][m][0]; acc[ai][bj][m][1] = xv[m][bj][1] + gv[bj][1] * acc[ai][bj][m][1];
;                           *(u32x4*)(op + (size_t)(ai * HALF + m * 16) * ldc + bj * HALF) = pk8(acc[ai][bj][m][0], acc[ai][bj][m][1]); }
.LBB0_666:
	s_lshl_b32 s6, s36, 5
	v_ashrrev_i32_e32 v128, 1, v187
	s_lshl_b32 s7, s4, 8
	v_and_b32_e32 v128, -8, v128
	s_or_b32 s6, s7, s6
	s_ashr_i32 s8, s3, 31
	v_add_u32_e32 v144, s6, v128
	s_lshr_b32 s6, s8, 20
	s_add_i32 s6, s3, s6
	s_ashr_i32 s6, s6, 12
	v_ashrrev_i32_e32 v145, 31, v144
	v_mov_b32_e32 v128, 0x1800
	v_mad_i64_i32 v[128:129], s[6:7], s6, v128, v[144:145]
	v_lshl_add_u64 v[172:173], v[128:129], 2, s[78:79]
	s_mov_b32 s9, 0x102000
	v_add_co_u32_e32 v128, vcc, s9, v172
	v_add_u32_e32 v146, s3, v186
	v_readlane_b32 s44, v254, 36
	v_addc_co_u32_e32 v129, vcc, 0, v173, vcc
	v_ashrrev_i32_e32 v147, 31, v146
	v_readlane_b32 s45, v254, 37
	v_readlane_b32 s48, v254, 40
	v_readlane_b32 s49, v254, 41
	s_barrier
	global_load_dwordx4 v[132:135], v[128:129], off
	v_lshlrev_b64 v[128:129], 12, v[146:147]
	s_mov_b64 s[48:49], s[44:45]
	s_mov_b64 s[6:7], 0x102000
	v_lshl_add_u64 v[128:129], s[48:49], 0, v[128:129]
	v_lshl_add_u64 v[184:185], v[144:145], 2, v[128:129]
	v_lshl_add_u64 v[128:129], v[172:173], 0, s[6:7]
	s_mov_b32 s6, 0x10000
	s_mov_b64 s[10:11], 0x10000
	v_add_co_u32_e32 v164, vcc, s6, v184
	v_lshl_add_u64 v[166:167], v[184:185], 0, s[10:11]
	s_nop 0
	v_addc_co_u32_e32 v165, vcc, 0, v185, vcc
	s_mov_b64 s[10:11], 0x10200
	s_mov_b32 s7, 0x20000
	global_load_dwordx4 v[148:151], v[184:185], off offset:16 nt
	global_load_dwordx4 v[152:155], v[184:185], off nt
	global_load_dwordx4 v[140:143], v[128:129], off offset:16
	global_load_dwordx4 v[136:139], v[128:129], off offset:512
	global_load_dwordx4 v[156:159], v[184:185], off offset:528 nt
	global_load_dwordx4 v[160:163], v[184:185], off offset:512 nt
	s_nop 0
	global_load_dwordx4 v[128:131], v[128:129], off offset:528
	s_mov_b32 s9, 0x80000
	global_load_dwordx4 v[190:193], v[164:165], off nt
	global_load_dwordx4 v[194:197], v[166:167], off offset:16 nt
	v_lshl_add_u64 v[166:167], v[184:185], 0, s[10:11]
	global_load_dwordx4 v[198:201], v[164:165], off offset:512 nt
	global_load_dwordx4 v[202:205], v[166:167], off offset:16 nt
	s_mov_b64 s[10:11], 0x20000
	v_add_co_u32_e32 v164, vcc, s7, v184
	v_lshl_add_u64 v[166:167], v[184:185], 0, s[10:11]
	s_nop 0
	v_addc_co_u32_e32 v165, vcc, 0, v185, vcc
	s_mov_b64 s[10:11], 0x20200
	global_load_dwordx4 v[206:209], v[164:165], off nt
	global_load_dwordx4 v[210:213], v[166:167], off offset:16 nt
	v_lshl_add_u64 v[166:167], v[184:185], 0, s[10:11]
	s_mov_b64 s[10:11], 0x30000
	s_mov_b32 s7, 0x30000
	global_load_dwordx4 v[214:217], v[164:165], off offset:512 nt
	global_load_dwordx4 v[218:221], v[166:167], off offset:16 nt
	v_add_co_u32_e32 v164, vcc, s7, v184
	v_lshl_add_u64 v[166:167], v[184:185], 0, s[10:11]
	s_nop 0
	v_addc_co_u32_e32 v165, vcc, 0, v185, vcc
	global_load_dwordx4 v[226:229], v[166:167], off offset:16 nt
	s_mov_b64 s[10:11], 0x30200
	global_load_dwordx4 v[222:225], v[164:165], off nt
	global_load_dwordx4 v[230:233], v[164:165], off offset:512 nt
	v_lshl_add_u64 v[164:165], v[184:185], 0, s[10:11]
	global_load_dwordx4 v[234:237], v[164:165], off offset:16 nt
	v_lshlrev_b64 v[166:167], 11, v[146:147]
	v_lshl_add_u64 v[166:167], s[18:19], 0, v[166:167]
	v_lshl_add_u64 v[182:183], v[144:145], 1, v[166:167]
	s_mov_b32 s7, 0x8000
	s_mov_b32 s10, 0xb0000
	s_lshl_b32 s5, s5, 10
	v_readlane_b32 s56, v254, 48
	v_readlane_b32 s57, v254, 49
	v_readlane_b32 s58, v254, 50
	v_readlane_b32 s59, v254, 51
	v_readlane_b32 s52, v254, 44
	v_readlane_b32 s53, v254, 45
	v_readlane_b32 s54, v254, 46
	v_readlane_b32 s55, v254, 47
	s_mov_b64 s[62:63], s[58:59]
	s_mov_b64 s[60:61], s[56:57]
	s_mov_b64 s[58:59], s[54:55]
	v_readlane_b32 s46, v254, 38
	v_readlane_b32 s47, v254, 39
	v_readlane_b32 s50, v254, 42
	v_readlane_b32 s51, v254, 43
	s_mov_b64 s[56:57], s[52:53]
	s_waitcnt vmcnt(0)
	v_pk_fma_f32 v[180:181], v[120:121], v[140:141], v[148:149]
	v_pk_fma_f32 v[174:175], v[126:127], v[134:135], v[154:155]
	v_pk_fma_f32 v[170:171], v[104:105], v[128:129], v[156:157]
	v_pk_fma_f32 v[176:177], v[124:125], v[132:133], v[152:153]
	v_pk_fma_f32 v[178:179], v[122:123], v[142:143], v[150:151]
	v_pk_fma_f32 v[156:157], v[108:109], v[140:141], v[194:195]
	v_add_co_u32_e32 v108, vcc, s7, v182
	v_cvt_pk_bf16_f32 v120, v176, v177
	v_cvt_pk_bf16_f32 v121, v174, v175
	v_cvt_pk_bf16_f32 v122, v180, v181
	v_cvt_pk_bf16_f32 v123, v178, v179
	s_nop 1
	v_addc_co_u32_e32 v109, vcc, 0, v183, vcc
	global_store_dwordx4 v[182:183], v[120:123], off
	v_pk_fma_f32 v[164:165], v[118:119], v[138:139], v[162:163]
	v_pk_fma_f32 v[166:167], v[116:117], v[136:137], v[160:161]
	v_pk_fma_f32 v[168:169], v[106:107], v[130:131], v[158:159]
	v_cvt_pk_bf16_f32 v104, v166, v167
	v_cvt_pk_bf16_f32 v105, v164, v165
	v_cvt_pk_bf16_f32 v106, v170, v171
	v_pk_fma_f32 v[120:121], v[92:93], v[140:141], v[210:211]
	v_cvt_pk_bf16_f32 v107, v168, v169
	v_add_co_u32_e32 v92, vcc, s6, v182
	global_store_dwordx4 v[182:183], v[104:107], off offset:256
	v_pk_fma_f32 v[160:161], v[114:115], v[134:135], v[192:193]
	v_pk_fma_f32 v[162:163], v[112:113], v[132:133], v[190:191]
	v_pk_fma_f32 v[158:159], v[110:111], v[142:143], v[196:197]
	v_cvt_pk_bf16_f32 v104, v162, v163
	v_cvt_pk_bf16_f32 v105, v160, v161
	v_cvt_pk_bf16_f32 v106, v156, v157
	v_pk_fma_f32 v[150:151], v[98:99], v[138:139], v[200:201]
	v_cvt_pk_bf16_f32 v107, v158, v159
	global_store_dwordx4 v[108:109], v[104:107], off
	v_pk_fma_f32 v[154:155], v[96:97], v[136:137], v[198:199]
	v_pk_fma_f32 v[148:149], v[90:91], v[130:131], v[204:205]
	v_pk_fma_f32 v[152:153], v[88:89], v[128:129], v[202:203]
	v_cvt_pk_bf16_f32 v88, v154, v155
	v_cvt_pk_bf16_f32 v89, v150, v151
	v_addc_co_u32_e32 v93, vcc, 0, v183, vcc
	v_cvt_pk_bf16_f32 v90, v152, v153
; __device__ __forceinline__ u32x4 pk8(const f32x4 a, const f32x4 b) { u32x4 q; q.x = cvt_pk_bf16(a[0], a[1]); q.y = cvt_pk_bf16(a[2], a[3]); q.z = cvt_pk_bf16(b[0], b[1]); q.w = cvt_pk_bf16(b[2], b[3]); return q; }
;     __device__ __forceinline__ void fused(f32x4 (&acc)[2][2][4][2], const Unit& u, int wr, int wc, int fr, int fq, PG8_LAS unsigned char* lds, int wid, int lane) const {
;     ...
;               for (int ai = 0; ai < 2; ++ai) {
; #pragma unroll
;                   for (int m = 0; m < 4; ++m)
; #pragma unroll
;                       for (int bj = 0; bj < 2; ++bj)
; #pragma unroll
;                           for (int n = 0; n < 2; ++n) xv[m][bj][n] = *(const f32x4*)(xp + (size_t)(ai * HALF + m * 16) * ldc + bj * HALF + n * 4);
; #pragma unroll
;                   for (int m = 0; m < 4; ++m)
; #pragma unroll
;                       for (int bj = 0; bj < 2; ++bj) { acc[ai][bj][m][0] = xv[m][bj][0] + gv[bj][0] * acc[ai][bj][m][0]; acc[ai][bj][m][1] = xv[m][bj][1] + gv[bj][1] * acc[ai][bj][m][1];
;                           *(u32x4*)(op + (size_t)(ai * HALF + m * 16) * ldc + bj * HALF) = pk8(acc[ai][bj][m][0], acc[ai][bj][m][1]); }
	v_cvt_pk_bf16_f32 v91, v148, v149
	s_mov_b32 s6, 0x18000
	global_store_dwordx4 v[108:109], v[88:91], off offset:256
	v_pk_fma_f32 v[124:125], v[102:103], v[134:135], v[208:209]
	v_pk_fma_f32 v[126:127], v[100:101], v[132:133], v[206:207]
	v_pk_fma_f32 v[122:123], v[94:95], v[142:143], v[212:213]
	v_cvt_pk_bf16_f32 v88, v126, v127
	v_cvt_pk_bf16_f32 v89, v124, v125
	v_cvt_pk_bf16_f32 v90, v120, v121
	v_pk_fma_f32 v[118:119], v[80:81], v[136:137], v[214:215]
	v_cvt_pk_bf16_f32 v91, v122, v123
	global_store_dwordx4 v[92:93], v[88:91], off
	v_pk_fma_f32 v[116:117], v[72:73], v[128:129], v[218:219]
	v_cvt_pk_bf16_f32 v72, v118, v119
	v_pk_fma_f32 v[104:105], v[76:77], v[140:141], v[226:227]
	v_add_co_u32_e32 v76, vcc, s6, v182
	v_pk_fma_f32 v[114:115], v[82:83], v[138:139], v[216:217]
	v_pk_fma_f32 v[112:113], v[74:75], v[130:131], v[220:221]
	v_cvt_pk_bf16_f32 v73, v114, v115
	v_cvt_pk_bf16_f32 v74, v116, v117
	v_pk_fma_f32 v[110:111], v[84:85], v[132:133], v[222:223]
	v_cvt_pk_bf16_f32 v75, v112, v113
	global_store_dwordx4 v[92:93], v[72:75], off offset:256
	v_addc_co_u32_e32 v77, vcc, 0, v183, vcc
	s_nop 0
	v_cvt_pk_bf16_f32 v72, v110, v111
	v_pk_fma_f32 v[108:109], v[86:87], v[134:135], v[224:225]
	v_pk_fma_f32 v[106:107], v[78:79], v[142:143], v[228:229]
	v_cvt_pk_bf16_f32 v73, v108, v109
	v_cvt_pk_bf16_f32 v74, v104, v105
	v_pk_fma_f32 v[90:91], v[70:71], v[138:139], v[232:233]
	v_cvt_pk_bf16_f32 v75, v106, v107
	global_store_dwordx4 v[76:77], v[72:75], off
	v_pk_fma_f32 v[94:95], v[68:69], v[136:137], v[230:231]
	v_pk_fma_f32 v[88:89], v[66:67], v[130:131], v[236:237]
	v_pk_fma_f32 v[92:93], v[64:65], v[128:129], v[234:235]
	v_cvt_pk_bf16_f32 v64, v94, v95
	v_cvt_pk_bf16_f32 v65, v90, v91
	s_mov_b64 s[6:7], 0x80000
	v_cvt_pk_bf16_f32 v66, v92, v93
	v_cvt_pk_bf16_f32 v67, v88, v89
	global_store_dwordx4 v[76:77], v[64:67], off offset:256
	v_add_co_u32_e32 v72, vcc, s9, v184
	v_lshl_add_u64 v[68:69], v[184:185], 0, s[6:7]
	s_nop 0
	v_addc_co_u32_e32 v73, vcc, 0, v185, vcc
	s_mov_b64 s[6:7], 0x80200
	s_mov_b32 s9, 0x90000
	global_load_dwordx4 v[64:67], v[72:73], off
	v_lshl_add_u64 v[76:77], v[184:185], 0, s[6:7]
	s_mov_b64 s[6:7], 0x90000
	v_add_co_u32_e32 v80, vcc, s9, v184
	v_lshl_add_u64 v[82:83], v[184:185], 0, s[6:7]
	s_nop 0
	v_addc_co_u32_e32 v81, vcc, 0, v185, vcc
	s_mov_b64 s[6:7], 0x90200
	s_mov_b32 s9, 0xa0000
	global_load_dwordx4 v[68:71], v[68:69], off offset:16
	s_nop 0
	global_load_dwordx4 v[72:75], v[72:73], off offset:512
	s_nop 0
	global_load_dwordx4 v[76:79], v[76:77], off offset:16
	s_waitcnt vmcnt(3)
	v_pk_fma_f32 v[102:103], v[60:61], v[132:133], v[64:65]
	global_load_dwordx4 v[190:193], v[80:81], off
	global_load_dwordx4 v[194:197], v[82:83], off offset:16
	v_lshl_add_u64 v[82:83], v[184:185], 0, s[6:7]
	global_load_dwordx4 v[198:201], v[80:81], off offset:512
	global_load_dwordx4 v[202:205], v[82:83], off offset:16
	s_mov_b64 s[6:7], 0xa0000
	v_add_co_u32_e32 v80, vcc, s9, v184
	v_lshl_add_u64 v[82:83], v[184:185], 0, s[6:7]
	s_nop 0
	v_addc_co_u32_e32 v81, vcc, 0, v185, vcc
	s_mov_b64 s[6:7], 0xa0200
	global_load_dwordx4 v[206:209], v[80:81], off
	global_load_dwordx4 v[210:213], v[82:83], off offset:16
	v_lshl_add_u64 v[82:83], v[184:185], 0, s[6:7]
	global_load_dwordx4 v[214:217], v[80:81], off offset:512
	global_load_dwordx4 v[218:221], v[82:83], off offset:16
	s_mov_b64 s[6:7], 0xb0000
	v_add_co_u32_e32 v80, vcc, s10, v184
	s_lshl_b32 s9, s36, 2
	s_nop 0
	v_addc_co_u32_e32 v81, vcc, 0, v185, vcc
	v_lshl_add_u64 v[82:83], v[184:185], 0, s[6:7]
	global_load_dwordx4 v[222:225], v[80:81], off
	global_load_dwordx4 v[226:229], v[82:83], off offset:16
	s_add_i32 s6, s9, 0
	s_add_i32 s5, s6, s5
	s_mov_b64 s[6:7], 0xb0200
	v_lshl_add_u64 v[82:83], v[184:185], 0, s[6:7]
	global_load_dwordx4 v[230:233], v[80:81], off offset:512
	global_load_dwordx4 v[234:237], v[82:83], off offset:16
	s_mov_b32 s6, 0x40000
	v_add_co_u32_e32 v60, vcc, s6, v182
	s_mov_b32 s6, 0x48000
	s_nop 0
	v_addc_co_u32_e32 v61, vcc, 0, v183, vcc
	s_waitcnt vmcnt(13)
	v_pk_fma_f32 v[86:87], v[48:49], v[136:137], v[72:73]
	v_pk_fma_f32 v[100:101], v[62:63], v[134:135], v[66:67]
	v_pk_fma_f32 v[96:97], v[56:57], v[140:141], v[68:69]
	v_cvt_pk_bf16_f32 v56, v102, v103
	v_cvt_pk_bf16_f32 v57, v100, v101
	v_pk_fma_f32 v[98:99], v[58:59], v[142:143], v[70:71]
	v_cvt_pk_bf16_f32 v58, v96, v97
	v_pk_fma_f32 v[82:83], v[50:51], v[138:139], v[74:75]
	v_cvt_pk_bf16_f32 v59, v98, v99
	global_store_dwordx4 v[60:61], v[56:59], off
	s_waitcnt vmcnt(13)
; __device__ __forceinline__ u32x4 pk8(const f32x4 a, const f32x4 b) { u32x4 q; q.x = cvt_pk_bf16(a[0], a[1]); q.y = cvt_pk_bf16(a[2], a[3]); q.z = cvt_pk_bf16(b[0], b[1]); q.w = cvt_pk_bf16(b[2], b[3]); return q; }
;     __device__ __forceinline__ bool run(const f32x4 (&v)[2][2][4][2], const Unit& u, int wr, int wc, int fr, int fq, PG8_LAS unsigned char* lds, int wid, int lane) const {
;     ...
;             for (int m = 0; m < 4; ++m) { float s = 0.f;
; #pragma unroll
;                 for (int bj = 0; bj < 2; ++bj)
; #pragma unroll
;                     for (int n = 0; n < 2; ++n) { const f32x4 x = v[ai][bj][m][n]; s += (x[0] * x[0] + x[1] * x[1]) + (x[2] * x[2] + x[3] * x[3]); }
;                 s += __shfl_xor(s, 16); s += __shfl_xor(s, 32);
;                 if (fq == 0) P[(ai * HALF + wr * 64 + m * 16 + fr) * 4 + wc] = s; }
;     __device__ __forceinline__ void fused(f32x4 (&acc)[2][2][4][2], const Unit& u, int wr, int wc, int fr, int fq, PG8_LAS unsigned char* lds, int wid, int lane) const {
;     ...
;                       for (int bj = 0; bj < 2; ++bj) { acc[ai][bj][m][0] = xv[m][bj][0] + gv[bj][0] * acc[ai][bj][m][0]; acc[ai][bj][m][1] = xv[m][bj][1] + gv[bj][1] * acc[ai][bj][m][1];
;                           *(u32x4*)(op + (size_t)(ai * HALF + m * 16) * ldc + bj * HALF) = pk8(acc[ai][bj][m][0], acc[ai][bj][m][1]); }
	v_pk_fma_f32 v[84:85], v[40:41], v[128:129], v[76:77]
	v_cvt_pk_bf16_f32 v40, v86, v87
	v_cvt_pk_bf16_f32 v41, v82, v83
	v_pk_fma_f32 v[80:81], v[42:43], v[130:131], v[78:79]
	v_cvt_pk_bf16_f32 v42, v84, v85
	s_waitcnt vmcnt(12)
	v_pk_fma_f32 v[76:77], v[54:55], v[134:135], v[192:193]
	s_waitcnt vmcnt(11)
	v_pk_fma_f32 v[72:73], v[44:45], v[140:141], v[194:195]
	v_add_co_u32_e32 v44, vcc, s6, v182
	s_mov_b32 s6, 0x50000
	s_nop 0
	v_addc_co_u32_e32 v45, vcc, 0, v183, vcc
	v_cvt_pk_bf16_f32 v43, v80, v81
	global_store_dwordx4 v[60:61], v[40:43], off offset:256
	v_pk_fma_f32 v[78:79], v[52:53], v[132:133], v[190:191]
	v_pk_fma_f32 v[74:75], v[46:47], v[142:143], v[196:197]
	v_cvt_pk_bf16_f32 v40, v78, v79
	s_waitcnt vmcnt(8)
	v_pk_fma_f32 v[56:57], v[28:29], v[140:141], v[210:211]
	v_add_co_u32_e32 v28, vcc, s6, v182
	v_cvt_pk_bf16_f32 v41, v76, v77
	s_mov_b32 s6, 0x58000
	s_nop 0
	v_addc_co_u32_e32 v29, vcc, 0, v183, vcc
	v_cvt_pk_bf16_f32 v42, v72, v73
	v_cvt_pk_bf16_f32 v43, v74, v75
	global_store_dwordx4 v[44:45], v[40:43], off
	v_pk_fma_f32 v[66:67], v[34:35], v[138:139], v[200:201]
	v_pk_fma_f32 v[70:71], v[32:33], v[136:137], v[198:199]
	v_pk_fma_f32 v[64:65], v[26:27], v[130:131], v[204:205]
	v_pk_fma_f32 v[68:69], v[24:25], v[128:129], v[202:203]
	v_cvt_pk_bf16_f32 v24, v70, v71
	v_cvt_pk_bf16_f32 v25, v66, v67
	s_waitcnt vmcnt(5)
	v_pk_fma_f32 v[40:41], v[12:13], v[140:141], v[226:227]
	v_cvt_pk_bf16_f32 v26, v68, v69
	v_cvt_pk_bf16_f32 v27, v64, v65
	v_add_co_u32_e32 v12, vcc, s6, v182
	global_store_dwordx4 v[44:45], v[24:27], off offset:256
	v_pk_fma_f32 v[60:61], v[38:39], v[134:135], v[208:209]
	v_pk_fma_f32 v[62:63], v[36:37], v[132:133], v[206:207]
	v_pk_fma_f32 v[58:59], v[30:31], v[142:143], v[212:213]
	v_cvt_pk_bf16_f32 v24, v62, v63
	v_cvt_pk_bf16_f32 v25, v60, v61
	v_cvt_pk_bf16_f32 v26, v56, v57
	v_pk_fma_f32 v[50:51], v[18:19], v[138:139], v[216:217]
	v_cvt_pk_bf16_f32 v27, v58, v59
	global_store_dwordx4 v[28:29], v[24:27], off
	v_pk_fma_f32 v[54:55], v[16:17], v[136:137], v[214:215]
	v_pk_fma_f32 v[48:49], v[10:11], v[130:131], v[220:221]
	v_pk_fma_f32 v[52:53], v[8:9], v[128:129], v[218:219]
	v_cvt_pk_bf16_f32 v8, v54, v55
	v_cvt_pk_bf16_f32 v9, v50, v51
	v_addc_co_u32_e32 v13, vcc, 0, v183, vcc
	v_cvt_pk_bf16_f32 v10, v52, v53
	v_cvt_pk_bf16_f32 v11, v48, v49
	global_store_dwordx4 v[28:29], v[8:11], off offset:256
	v_pk_fma_f32 v[44:45], v[22:23], v[134:135], v[224:225]
	v_pk_fma_f32 v[46:47], v[20:21], v[132:133], v[222:223]
	v_pk_fma_f32 v[42:43], v[14:15], v[142:143], v[228:229]
	v_cvt_pk_bf16_f32 v8, v46, v47
	v_cvt_pk_bf16_f32 v9, v44, v45
	v_cvt_pk_bf16_f32 v10, v40, v41
	s_waitcnt vmcnt(7)
	v_pk_fma_f32 v[34:35], v[6:7], v[138:139], v[232:233]
	v_cvt_pk_bf16_f32 v11, v42, v43
	global_store_dwordx4 v[12:13], v[8:11], off
	v_pk_fma_f32 v[38:39], v[4:5], v[136:137], v[230:231]
	s_waitcnt vmcnt(7)
	v_pk_fma_f32 v[32:33], v[2:3], v[130:131], v[236:237]
	v_pk_fma_f32 v[36:37], v[0:1], v[128:129], v[234:235]
	v_cvt_pk_bf16_f32 v0, v38, v39
	v_cvt_pk_bf16_f32 v1, v34, v35
	v_mul_f32_e32 v4, v175, v175
	v_cvt_pk_bf16_f32 v2, v36, v37
	v_cvt_pk_bf16_f32 v3, v32, v33
	global_store_dwordx4 v[12:13], v[0:3], off offset:256
	v_fmac_f32_e32 v4, v174, v174
	v_mul_f32_e32 v5, v179, v179
	v_mul_f32_e32 v3, v177, v177
	v_fmac_f32_e32 v3, v176, v176
	v_add_f32_e32 v3, v3, v4
	v_mul_f32_e32 v4, v181, v181
	v_fmac_f32_e32 v4, v180, v180
	v_fmac_f32_e32 v5, v178, v178
	v_add_f32_e32 v4, v4, v5
	v_mbcnt_lo_u32_b32 v0, -1, 0
	v_add_f32_e32 v3, v3, v4
	v_mul_f32_e32 v4, v167, v167
	v_mul_f32_e32 v5, v165, v165
	v_mbcnt_hi_u32_b32 v1, -1, v0
	v_fmac_f32_e32 v4, v166, v166
	v_fmac_f32_e32 v5, v164, v164
	v_and_b32_e32 v2, 64, v1
	v_add_f32_e32 v4, v4, v5
	v_xor_b32_e32 v0, 16, v1
	v_add_u32_e32 v2, 64, v2
	v_add_f32_e32 v3, v3, v4
	v_mul_f32_e32 v4, v171, v171
	v_mul_f32_e32 v5, v169, v169
	v_cmp_lt_i32_e32 vcc, v0, v2
	v_fmac_f32_e32 v4, v170, v170
	v_fmac_f32_e32 v5, v168, v168
	v_cndmask_b32_e32 v0, v1, v0, vcc
	v_add_f32_e32 v4, v4, v5
	v_lshlrev_b32_e32 v0, 2, v0
	v_add_f32_e32 v3, v3, v4
	v_mov_b32_e32 v4, v3
	s_nop 1
	v_permlane16_swap_b32_e32 v4, v3
	v_xor_b32_e32 v5, 32, v1
	v_cmp_lt_i32_e32 vcc, v5, v2
	s_waitcnt lgkmcnt(0)
	v_add_f32_e32 v3, v3, v4
	v_cndmask_b32_e32 v1, v1, v5, vcc
	v_lshlrev_b32_e32 v2, 2, v1
	v_mov_b32_e32 v4, v3
	s_nop 1
	v_permlane32_swap_b32_e32 v4, v3
	v_cmp_gt_u32_e32 vcc, 16, v187
	v_add_u32_e32 v1, s5, v188
	s_and_saveexec_b64 s[6:7], vcc
	s_cbranch_execz .LBB0_668
	s_waitcnt lgkmcnt(0)
	v_add_f32_e32 v3, v3, v4
	ds_write_b32 v1, v3

; #define GAS __attribute__((address_space(1)))
; #define LAS __attribute__((address_space(3)))
; __device__ __forceinline__ float bf_lo(unsigned w) { return __uint_as_float(w << 16); }
; __device__ __forceinline__ float bf_hi(unsigned w) { return __uint_as_float(w & 0xffff0000u); }
; __device__ __forceinline__ void route_rows(Frame& F, const bf16* xin, const float* g, const float* shift, const float* scale, const float* w_router, const float* b_router,
;                                            unsigned char* XS, float* wl, int* posi, gu32* cnt) {
;     ...
;         for (int gq = 0; gq < 2; ++gq) {
;             u32x2r xb[4][4];
; #pragma unroll
;             for (int r = 0; r < 4; ++r) { const GAS u32x2r* xr = (const GAS u32x2r*)(xin + (size_t)(row0 + gq * 4 + r) * D) + lane;
; #pragma unroll
;                 for (int j = 0; j < 4; ++j) xb[r][j] = xr[64 * j]; }
;             float lg[32], ss[4];
; #pragma unroll
;             for (int i = 0; i < 32; ++i) lg[i] = 0.f;
; #pragma unroll
;             for (int i = 0; i < 4; ++i) ss[i] = 0.f;
; #pragma unroll
;             for (int j = 0; j < 4; ++j)
; #pragma unroll
;                 for (int i = 0; i < 4; ++i) { const LAS f32x4* wq = (const LAS f32x4*)(wr + (size_t)(4 * lane + 256 * j + i) * 8); const f32x4 wa = wq[0], wb = wq[1]; const float gsv = gs[j][i];
; #pragma unroll
;                     for (int r = 0; r < 4; ++r) { const unsigned wd = (i < 2) ? xb[r][j].x : xb[r][j].y; const float xv = (i & 1) ? bf_hi(wd) : bf_lo(wd), xt = xv * gsv;
;                         ss[r] += xv * xv;
;                         lg[8 * r + 0] += xt * wa.x; lg[8 * r + 1] += xt * wa.y; lg[8 * r + 2] += xt * wa.z; lg[8 * r + 3] += xt * wa.w; lg[8 * r + 4] += xt * wb.x; lg[8 * r + 5] += xt * wb.y; lg[8 * r + 6] += xt * wb.z; lg[8 * r + 7] += xt * wb.w; } }
.LBB0_1649:
	s_lshl_b32 s4, s45, 2
	s_or_b32 s4, s4, s44
	s_ashr_i32 s5, s4, 31
	s_lshl_b64 s[12:13], s[4:5], 11
	v_lshl_add_u64 v[22:23], v[20:21], 0, s[12:13]
	s_or_b32 s12, s4, 1
	s_ashr_i32 s13, s12, 31
	s_lshl_b64 s[12:13], s[12:13], 11
	v_lshl_add_u64 v[28:29], v[20:21], 0, s[12:13]
	s_or_b32 s12, s4, 2
	s_ashr_i32 s13, s12, 31
	s_or_b32 s4, s4, 3
	s_lshl_b64 s[12:13], s[12:13], 11
	s_ashr_i32 s5, s4, 31
	v_lshl_add_u64 v[30:31], v[20:21], 0, s[12:13]
	s_lshl_b64 s[4:5], s[4:5], 11
	global_load_dwordx2 v[50:51], v[22:23], off nt
	global_load_dwordx2 v[46:47], v[28:29], off nt
	global_load_dwordx2 v[44:45], v[30:31], off nt
	v_lshl_add_u64 v[36:37], v[20:21], 0, s[4:5]
	global_load_dwordx2 v[38:39], v[36:37], off nt
	ds_read_b128 v[64:67], v116
	ds_read_b128 v[76:79], v116 offset:16
	ds_read_b128 v[80:83], v116 offset:32
	ds_read_b128 v[92:95], v116 offset:48
	global_load_dwordx2 v[74:75], v[22:23], off offset:512 nt
	global_load_dwordx2 v[90:91], v[22:23], off offset:1024 nt
	global_load_dwordx2 v[58:59], v[22:23], off offset:1536 nt
	global_load_dwordx2 v[72:73], v[28:29], off offset:512 nt
	global_load_dwordx2 v[88:89], v[28:29], off offset:1024 nt
	global_load_dwordx2 v[62:63], v[28:29], off offset:1536 nt
	global_load_dwordx2 v[70:71], v[30:31], off offset:512 nt
	global_load_dwordx2 v[86:87], v[30:31], off offset:1024 nt
	global_load_dwordx2 v[54:55], v[30:31], off offset:1536 nt
	global_load_dwordx2 v[68:69], v[36:37], off offset:512 nt
	global_load_dwordx2 v[84:85], v[36:37], off offset:1024 nt
	global_load_dwordx2 v[56:57], v[36:37], off offset:1536 nt
	s_waitcnt vmcnt(9)
	v_and_b32_e32 v106, 0xffff0000, v59
	v_lshlrev_b32_e32 v109, 16, v59
	v_mov_b32_e32 v108, v106
	v_lshlrev_b32_e32 v36, 16, v50
	v_and_b32_e32 v37, 0xffff0000, v50
	v_lshlrev_b32_e32 v28, 16, v44
	v_mul_f32_e32 v23, v40, v36
	v_lshlrev_b32_e32 v30, 16, v46
	v_lshlrev_b32_e32 v22, 16, v38
	v_mul_f32_e32 v31, v40, v28
	v_mul_f32_e32 v29, v41, v37
	s_waitcnt lgkmcnt(3)
	v_fma_f32 v146, v23, v64, 0
	v_fma_f32 v144, v23, v65, 0
	v_fma_f32 v142, v23, v66, 0
	v_fma_f32 v140, v23, v67, 0
	s_waitcnt lgkmcnt(2)
	v_fma_f32 v138, v23, v76, 0
	v_fma_f32 v136, v23, v77, 0
	v_fma_f32 v134, v23, v78, 0
	v_fma_f32 v132, v23, v79, 0
	v_mul_f32_e32 v23, v40, v30
	v_mul_f32_e32 v50, v40, v22
	v_fma_f32 v149, v31, v64, 0
	v_fma_f32 v148, v31, v65, 0
	v_fma_f32 v147, v31, v66, 0
	v_fma_f32 v145, v31, v67, 0
	v_fma_f32 v143, v31, v76, 0
	v_fma_f32 v141, v31, v77, 0
	v_fma_f32 v139, v31, v78, 0
	v_fma_f32 v137, v31, v79, 0
	v_and_b32_e32 v31, 0xffff0000, v46
	v_fma_f32 v130, v23, v64, 0
	v_fma_f32 v129, v23, v65, 0
	v_fma_f32 v128, v23, v66, 0
	v_fma_f32 v124, v23, v67, 0
	v_fma_f32 v123, v23, v76, 0
	v_fma_f32 v122, v23, v77, 0
	v_fma_f32 v119, v23, v78, 0
	v_fma_f32 v107, v23, v79, 0
	v_fma_f32 v135, v50, v64, 0
	v_fma_f32 v133, v50, v65, 0
	v_fma_f32 v131, v50, v66, 0
	v_fma_f32 v127, v50, v67, 0
	v_fma_f32 v126, v50, v76, 0
	v_fma_f32 v125, v50, v77, 0
	v_fma_f32 v121, v50, v78, 0
	v_fma_f32 v120, v50, v79, 0
	s_waitcnt lgkmcnt(1)
	v_fmac_f32_e32 v146, v29, v80
	v_fmac_f32_e32 v144, v29, v81
	v_fmac_f32_e32 v142, v29, v82
	v_fmac_f32_e32 v140, v29, v83
	s_waitcnt lgkmcnt(0)
	v_fmac_f32_e32 v138, v29, v92
	v_fmac_f32_e32 v136, v29, v93
	v_fmac_f32_e32 v134, v29, v94
	v_fmac_f32_e32 v132, v29, v95
	v_mul_f32_e32 v23, v41, v31
	v_and_b32_e32 v29, 0xffff0000, v44
	ds_read_b128 v[64:67], v116 offset:64
	ds_read_b128 v[76:79], v116 offset:80
	v_fmac_f32_e32 v130, v23, v80
	v_fmac_f32_e32 v129, v23, v81
	v_fmac_f32_e32 v128, v23, v82
	v_fmac_f32_e32 v124, v23, v83
	v_fmac_f32_e32 v123, v23, v92
	v_fmac_f32_e32 v122, v23, v93
	v_fmac_f32_e32 v119, v23, v94
	v_fmac_f32_e32 v107, v23, v95
	v_mul_f32_e32 v23, v41, v29
	v_fmac_f32_e32 v149, v23, v80
	v_fmac_f32_e32 v148, v23, v81
	v_fmac_f32_e32 v147, v23, v82
	v_fmac_f32_e32 v145, v23, v83
	v_fmac_f32_e32 v143, v23, v92
	v_fmac_f32_e32 v141, v23, v93
	v_fmac_f32_e32 v139, v23, v94
	v_fmac_f32_e32 v137, v23, v95
	v_and_b32_e32 v23, 0xffff0000, v38
	v_mul_f32_e32 v38, v41, v23
	v_lshlrev_b32_e32 v50, 16, v51
	v_fmac_f32_e32 v135, v38, v80
	v_fmac_f32_e32 v133, v38, v81
	v_fmac_f32_e32 v131, v38, v82
	v_fmac_f32_e32 v127, v38, v83
	v_fmac_f32_e32 v126, v38, v92
	v_fmac_f32_e32 v125, v38, v93
	v_fmac_f32_e32 v121, v38, v94
	v_fmac_f32_e32 v120, v38, v95
	v_mul_f32_e32 v38, v42, v50
	v_lshlrev_b32_e32 v46, 16, v47
	s_waitcnt lgkmcnt(1)
	v_fmac_f32_e32 v146, v38, v64
	v_fmac_f32_e32 v144, v38, v65
	v_fmac_f32_e32 v142, v38, v66
	v_fmac_f32_e32 v140, v38, v67
	s_waitcnt lgkmcnt(0)
	v_fmac_f32_e32 v138, v38, v76
	v_fmac_f32_e32 v136, v38, v77
	v_fmac_f32_e32 v134, v38, v78
	v_fmac_f32_e32 v132, v38, v79
	v_mul_f32_e32 v38, v42, v46
	v_lshlrev_b32_e32 v44, 16, v45
	v_fmac_f32_e32 v130, v38, v64
	v_fmac_f32_e32 v129, v38, v65
	v_fmac_f32_e32 v128, v38, v66
	v_fmac_f32_e32 v124, v38, v67
	v_fmac_f32_e32 v123, v38, v76
	v_fmac_f32_e32 v122, v38, v77
	v_fmac_f32_e32 v119, v38, v78
	v_fmac_f32_e32 v107, v38, v79
	v_mul_f32_e32 v38, v42, v44
	v_fmac_f32_e32 v149, v38, v64
	v_fmac_f32_e32 v148, v38, v65
	v_fmac_f32_e32 v147, v38, v66
	v_fmac_f32_e32 v145, v38, v67
	v_fmac_f32_e32 v143, v38, v76
	v_fmac_f32_e32 v141, v38, v77
	v_fmac_f32_e32 v139, v38, v78
	v_fmac_f32_e32 v137, v38, v79
	v_lshlrev_b32_e32 v38, 16, v39
	v_mul_f32_e32 v52, v42, v38
	v_fmac_f32_e32 v135, v52, v64
	v_fmac_f32_e32 v133, v52, v65
	v_fmac_f32_e32 v131, v52, v66
	v_fmac_f32_e32 v127, v52, v67
	v_fmac_f32_e32 v126, v52, v76
	v_fmac_f32_e32 v125, v52, v77
	v_fmac_f32_e32 v121, v52, v78
	v_fmac_f32_e32 v120, v52, v79
	ds_read_b128 v[64:67], v116 offset:96
	ds_read_b128 v[76:79], v116 offset:112
	v_and_b32_e32 v51, 0xffff0000, v51
	v_mul_f32_e32 v52, v43, v51
	v_and_b32_e32 v47, 0xffff0000, v47
	s_waitcnt lgkmcnt(1)
; #define LAS __attribute__((address_space(3)))
; __device__ __forceinline__ float bf_lo(unsigned w) { return __uint_as_float(w << 16); }
; __device__ __forceinline__ float bf_hi(unsigned w) { return __uint_as_float(w & 0xffff0000u); }
; __device__ __forceinline__ void route_rows(Frame& F, const bf16* xin, const float* g, const float* shift, const float* scale, const float* w_router, const float* b_router,
;                                            unsigned char* XS, float* wl, int* posi, gu32* cnt) {
;     ...
; #pragma unroll
;             for (int j = 0; j < 4; ++j)
; #pragma unroll
;                 for (int i = 0; i < 4; ++i) { const LAS f32x4* wq = (const LAS f32x4*)(wr + (size_t)(4 * lane + 256 * j + i) * 8); const f32x4 wa = wq[0], wb = wq[1]; const float gsv = gs[j][i];
; #pragma unroll
;                     for (int r = 0; r < 4; ++r) { const unsigned wd = (i < 2) ? xb[r][j].x : xb[r][j].y; const float xv = (i & 1) ? bf_hi(wd) : bf_lo(wd), xt = xv * gsv;
;                         ss[r] += xv * xv;
;                         lg[8 * r + 0] += xt * wa.x; lg[8 * r + 1] += xt * wa.y; lg[8 * r + 2] += xt * wa.z; lg[8 * r + 3] += xt * wa.w; lg[8 * r + 4] += xt * wb.x; lg[8 * r + 5] += xt * wb.y; lg[8 * r + 6] += xt * wb.z; lg[8 * r + 7] += xt * wb.w; } }
	v_fmac_f32_e32 v146, v52, v64
	v_fmac_f32_e32 v144, v52, v65
	v_fmac_f32_e32 v142, v52, v66
	v_fmac_f32_e32 v140, v52, v67
	s_waitcnt lgkmcnt(0)
	v_fmac_f32_e32 v138, v52, v76
	v_fmac_f32_e32 v136, v52, v77
	v_fmac_f32_e32 v134, v52, v78
	v_fmac_f32_e32 v132, v52, v79
	v_mul_f32_e32 v52, v43, v47
	v_and_b32_e32 v45, 0xffff0000, v45
	v_fmac_f32_e32 v130, v52, v64
	v_fmac_f32_e32 v129, v52, v65
	v_fmac_f32_e32 v128, v52, v66
	v_fmac_f32_e32 v124, v52, v67
	v_fmac_f32_e32 v123, v52, v76
	v_fmac_f32_e32 v122, v52, v77
	v_fmac_f32_e32 v119, v52, v78
	v_fmac_f32_e32 v107, v52, v79
	v_mul_f32_e32 v52, v43, v45
	v_and_b32_e32 v39, 0xffff0000, v39
	v_fmac_f32_e32 v149, v52, v64
	v_fmac_f32_e32 v148, v52, v65
	v_fmac_f32_e32 v147, v52, v66
	v_fmac_f32_e32 v145, v52, v67
	v_fmac_f32_e32 v143, v52, v76
	v_fmac_f32_e32 v141, v52, v77
	v_fmac_f32_e32 v139, v52, v78
	v_fmac_f32_e32 v137, v52, v79
	v_mul_f32_e32 v52, v43, v39
	v_fmac_f32_e32 v126, v52, v76
	v_fmac_f32_e32 v125, v52, v77
	v_fmac_f32_e32 v121, v52, v78
	v_fmac_f32_e32 v120, v52, v79
	ds_read_b128 v[76:79], v116 offset:8192
	ds_read_b128 v[80:83], v116 offset:8208
	v_fmac_f32_e32 v131, v52, v66
	v_lshlrev_b32_e32 v66, 16, v74
	v_fmac_f32_e32 v135, v52, v64
	v_fmac_f32_e32 v133, v52, v65
	v_fmac_f32_e32 v127, v52, v67
	v_mul_f32_e32 v52, v32, v66
	s_waitcnt vmcnt(8)
	v_lshlrev_b32_e32 v64, 16, v72
	s_waitcnt lgkmcnt(1)
	v_fmac_f32_e32 v146, v52, v76
	v_fmac_f32_e32 v144, v52, v77
	v_fmac_f32_e32 v142, v52, v78
	v_fmac_f32_e32 v140, v52, v79
	s_waitcnt lgkmcnt(0)
	v_fmac_f32_e32 v138, v52, v80
	v_fmac_f32_e32 v136, v52, v81
	v_fmac_f32_e32 v134, v52, v82
	v_fmac_f32_e32 v132, v52, v83
	v_mul_f32_e32 v52, v32, v64
	s_waitcnt vmcnt(5)
	v_lshlrev_b32_e32 v60, 16, v70
	v_fmac_f32_e32 v130, v52, v76
	v_fmac_f32_e32 v129, v52, v77
	v_fmac_f32_e32 v128, v52, v78
	v_fmac_f32_e32 v124, v52, v79
	v_fmac_f32_e32 v123, v52, v80
	v_fmac_f32_e32 v122, v52, v81
	v_fmac_f32_e32 v119, v52, v82
	v_fmac_f32_e32 v107, v52, v83
	v_mul_f32_e32 v52, v32, v60
	v_fmac_f32_e32 v149, v52, v76
	v_fmac_f32_e32 v148, v52, v77
	v_fmac_f32_e32 v147, v52, v78
	v_fmac_f32_e32 v145, v52, v79
	v_fmac_f32_e32 v143, v52, v80
	v_fmac_f32_e32 v141, v52, v81
	v_fmac_f32_e32 v139, v52, v82
	v_fmac_f32_e32 v137, v52, v83
	s_waitcnt vmcnt(2)
	v_lshlrev_b32_e32 v52, 16, v68
	v_mul_f32_e32 v53, v32, v52
	v_fmac_f32_e32 v135, v53, v76
	v_fmac_f32_e32 v133, v53, v77
	v_fmac_f32_e32 v131, v53, v78
	v_fmac_f32_e32 v127, v53, v79
	v_fmac_f32_e32 v126, v53, v80
	v_fmac_f32_e32 v125, v53, v81
	v_fmac_f32_e32 v121, v53, v82
	v_fmac_f32_e32 v120, v53, v83
	ds_read_b128 v[76:79], v116 offset:8224
	ds_read_b128 v[80:83], v116 offset:8240
	v_and_b32_e32 v67, 0xffff0000, v74
	v_mul_f32_e32 v53, v33, v67
	v_and_b32_e32 v65, 0xffff0000, v72
	s_waitcnt lgkmcnt(1)
	v_fmac_f32_e32 v146, v53, v76
	v_fmac_f32_e32 v144, v53, v77
	v_fmac_f32_e32 v142, v53, v78
	v_fmac_f32_e32 v140, v53, v79
	s_waitcnt lgkmcnt(0)
	v_fmac_f32_e32 v138, v53, v80
	v_fmac_f32_e32 v136, v53, v81
	v_fmac_f32_e32 v134, v53, v82
	v_fmac_f32_e32 v132, v53, v83
	v_mul_f32_e32 v53, v33, v65
	v_and_b32_e32 v61, 0xffff0000, v70
	v_fmac_f32_e32 v130, v53, v76
	v_fmac_f32_e32 v129, v53, v77
	v_fmac_f32_e32 v128, v53, v78
	v_fmac_f32_e32 v124, v53, v79
	v_fmac_f32_e32 v123, v53, v80
	v_fmac_f32_e32 v122, v53, v81
	v_fmac_f32_e32 v119, v53, v82
	v_fmac_f32_e32 v107, v53, v83
	v_mul_f32_e32 v53, v33, v61
	v_fmac_f32_e32 v149, v53, v76
	v_fmac_f32_e32 v148, v53, v77
	v_fmac_f32_e32 v147, v53, v78
	v_fmac_f32_e32 v145, v53, v79
	v_fmac_f32_e32 v143, v53, v80
	v_fmac_f32_e32 v141, v53, v81
	v_fmac_f32_e32 v139, v53, v82
	v_fmac_f32_e32 v137, v53, v83
	v_and_b32_e32 v53, 0xffff0000, v68
	v_mul_f32_e32 v68, v33, v53
	v_fmac_f32_e32 v135, v68, v76
	v_fmac_f32_e32 v133, v68, v77
	v_fmac_f32_e32 v131, v68, v78
	v_fmac_f32_e32 v127, v68, v79
	v_fmac_f32_e32 v126, v68, v80
	v_fmac_f32_e32 v125, v68, v81
	v_fmac_f32_e32 v121, v68, v82
	v_fmac_f32_e32 v120, v68, v83
	ds_read_b128 v[76:79], v116 offset:8256
	ds_read_b128 v[80:83], v116 offset:8272
	v_lshlrev_b32_e32 v74, 16, v75
	v_mul_f32_e32 v68, v34, v74
	v_lshlrev_b32_e32 v72, 16, v73
	s_waitcnt lgkmcnt(1)
	v_fmac_f32_e32 v146, v68, v76
	v_fmac_f32_e32 v144, v68, v77
	v_fmac_f32_e32 v142, v68, v78
	v_fmac_f32_e32 v140, v68, v79
	s_waitcnt lgkmcnt(0)
	v_fmac_f32_e32 v138, v68, v80
	v_fmac_f32_e32 v136, v68, v81
	v_fmac_f32_e32 v134, v68, v82
	v_fmac_f32_e32 v132, v68, v83
	v_mul_f32_e32 v68, v34, v72
	v_lshlrev_b32_e32 v70, 16, v71
	v_fmac_f32_e32 v130, v68, v76
	v_fmac_f32_e32 v129, v68, v77
	v_fmac_f32_e32 v128, v68, v78
	v_fmac_f32_e32 v124, v68, v79
	v_fmac_f32_e32 v123, v68, v80
	v_fmac_f32_e32 v122, v68, v81
	v_fmac_f32_e32 v119, v68, v82
	v_fmac_f32_e32 v107, v68, v83
	v_mul_f32_e32 v68, v34, v70
	v_fmac_f32_e32 v149, v68, v76
	v_fmac_f32_e32 v148, v68, v77
	v_fmac_f32_e32 v147, v68, v78
	v_fmac_f32_e32 v145, v68, v79
	v_fmac_f32_e32 v143, v68, v80
	v_fmac_f32_e32 v141, v68, v81
	v_fmac_f32_e32 v139, v68, v82
	v_fmac_f32_e32 v137, v68, v83
	v_lshlrev_b32_e32 v68, 16, v69
	v_mul_f32_e32 v92, v34, v68
	v_fmac_f32_e32 v135, v92, v76
	v_fmac_f32_e32 v133, v92, v77
	v_fmac_f32_e32 v131, v92, v78
	v_fmac_f32_e32 v127, v92, v79
	v_fmac_f32_e32 v126, v92, v80
	v_fmac_f32_e32 v125, v92, v81
	v_fmac_f32_e32 v121, v92, v82
	v_fmac_f32_e32 v120, v92, v83
	ds_read_b128 v[76:79], v116 offset:8288
	ds_read_b128 v[80:83], v116 offset:8304
	v_and_b32_e32 v75, 0xffff0000, v75
	v_mul_f32_e32 v92, v35, v75
	v_and_b32_e32 v73, 0xffff0000, v73
	s_waitcnt lgkmcnt(1)
	v_fmac_f32_e32 v146, v92, v76
	v_fmac_f32_e32 v144, v92, v77
	v_fmac_f32_e32 v142, v92, v78
	v_fmac_f32_e32 v140, v92, v79
	s_waitcnt lgkmcnt(0)
; #define LAS __attribute__((address_space(3)))
; __device__ __forceinline__ float bf_lo(unsigned w) { return __uint_as_float(w << 16); }
; __device__ __forceinline__ float bf_hi(unsigned w) { return __uint_as_float(w & 0xffff0000u); }
; __device__ __forceinline__ void route_rows(Frame& F, const bf16* xin, const float* g, const float* shift, const float* scale, const float* w_router, const float* b_router,
;                                            unsigned char* XS, float* wl, int* posi, gu32* cnt) {
;     ...
; #pragma unroll
;             for (int j = 0; j < 4; ++j)
; #pragma unroll
;                 for (int i = 0; i < 4; ++i) { const LAS f32x4* wq = (const LAS f32x4*)(wr + (size_t)(4 * lane + 256 * j + i) * 8); const f32x4 wa = wq[0], wb = wq[1]; const float gsv = gs[j][i];
; #pragma unroll
;                     for (int r = 0; r < 4; ++r) { const unsigned wd = (i < 2) ? xb[r][j].x : xb[r][j].y; const float xv = (i & 1) ? bf_hi(wd) : bf_lo(wd), xt = xv * gsv;
;                         ss[r] += xv * xv;
;                         lg[8 * r + 0] += xt * wa.x; lg[8 * r + 1] += xt * wa.y; lg[8 * r + 2] += xt * wa.z; lg[8 * r + 3] += xt * wa.w; lg[8 * r + 4] += xt * wb.x; lg[8 * r + 5] += xt * wb.y; lg[8 * r + 6] += xt * wb.z; lg[8 * r + 7] += xt * wb.w; } }
	v_fmac_f32_e32 v138, v92, v80
	v_fmac_f32_e32 v136, v92, v81
	v_fmac_f32_e32 v134, v92, v82
	v_fmac_f32_e32 v132, v92, v83
	v_mul_f32_e32 v92, v35, v73
	v_and_b32_e32 v71, 0xffff0000, v71
	v_fmac_f32_e32 v130, v92, v76
	v_fmac_f32_e32 v129, v92, v77
	v_fmac_f32_e32 v128, v92, v78
	v_fmac_f32_e32 v124, v92, v79
	v_fmac_f32_e32 v123, v92, v80
	v_fmac_f32_e32 v122, v92, v81
	v_fmac_f32_e32 v119, v92, v82
	v_fmac_f32_e32 v107, v92, v83
	v_mul_f32_e32 v92, v35, v71
	v_and_b32_e32 v69, 0xffff0000, v69
	v_fmac_f32_e32 v149, v92, v76
	v_fmac_f32_e32 v148, v92, v77
	v_fmac_f32_e32 v147, v92, v78
	v_fmac_f32_e32 v145, v92, v79
	v_fmac_f32_e32 v143, v92, v80
	v_fmac_f32_e32 v141, v92, v81
	v_fmac_f32_e32 v139, v92, v82
	v_fmac_f32_e32 v137, v92, v83
	v_mul_f32_e32 v92, v35, v69
	v_fmac_f32_e32 v135, v92, v76
	v_fmac_f32_e32 v133, v92, v77
	v_fmac_f32_e32 v131, v92, v78
	v_fmac_f32_e32 v127, v92, v79
	v_fmac_f32_e32 v126, v92, v80
	v_fmac_f32_e32 v125, v92, v81
	v_fmac_f32_e32 v121, v92, v82
	v_fmac_f32_e32 v120, v92, v83
	ds_read_b128 v[92:95], v116 offset:16384
	ds_read_b128 v[96:99], v116 offset:16400
	v_lshlrev_b32_e32 v82, 16, v90
	v_mul_f32_e32 v76, v24, v82
	v_lshlrev_b32_e32 v80, 16, v88
	s_waitcnt lgkmcnt(1)
	v_fmac_f32_e32 v146, v76, v92
	v_fmac_f32_e32 v144, v76, v93
	v_fmac_f32_e32 v142, v76, v94
	v_fmac_f32_e32 v140, v76, v95
	s_waitcnt lgkmcnt(0)
	v_fmac_f32_e32 v138, v76, v96
	v_fmac_f32_e32 v136, v76, v97
	v_fmac_f32_e32 v134, v76, v98
	v_fmac_f32_e32 v132, v76, v99
	v_mul_f32_e32 v76, v24, v80
	v_lshlrev_b32_e32 v78, 16, v86
	v_fmac_f32_e32 v130, v76, v92
	v_fmac_f32_e32 v129, v76, v93
	v_fmac_f32_e32 v128, v76, v94
	v_fmac_f32_e32 v124, v76, v95
	v_fmac_f32_e32 v123, v76, v96
	v_fmac_f32_e32 v122, v76, v97
	v_fmac_f32_e32 v119, v76, v98
	v_fmac_f32_e32 v107, v76, v99
	v_mul_f32_e32 v76, v24, v78
	v_fmac_f32_e32 v149, v76, v92
	v_fmac_f32_e32 v148, v76, v93
	v_fmac_f32_e32 v147, v76, v94
	v_fmac_f32_e32 v145, v76, v95
	v_fmac_f32_e32 v143, v76, v96
	v_fmac_f32_e32 v141, v76, v97
	v_fmac_f32_e32 v139, v76, v98
	v_fmac_f32_e32 v137, v76, v99
	s_waitcnt vmcnt(1)
	v_lshlrev_b32_e32 v76, 16, v84
	v_mul_f32_e32 v77, v24, v76
	v_fmac_f32_e32 v135, v77, v92
	v_fmac_f32_e32 v133, v77, v93
	v_fmac_f32_e32 v131, v77, v94
	v_fmac_f32_e32 v127, v77, v95
	v_fmac_f32_e32 v126, v77, v96
	v_fmac_f32_e32 v125, v77, v97
	v_fmac_f32_e32 v121, v77, v98
	v_fmac_f32_e32 v120, v77, v99
	ds_read_b128 v[92:95], v116 offset:16416
	ds_read_b128 v[96:99], v116 offset:16432
	v_and_b32_e32 v83, 0xffff0000, v90
	v_mul_f32_e32 v77, v25, v83
	v_and_b32_e32 v81, 0xffff0000, v88
	s_waitcnt lgkmcnt(1)
	v_fmac_f32_e32 v146, v77, v92
	v_fmac_f32_e32 v144, v77, v93
	v_fmac_f32_e32 v142, v77, v94
	v_fmac_f32_e32 v140, v77, v95
	s_waitcnt lgkmcnt(0)
	v_fmac_f32_e32 v138, v77, v96
	v_fmac_f32_e32 v136, v77, v97
	v_fmac_f32_e32 v134, v77, v98
	v_fmac_f32_e32 v132, v77, v99
	v_mul_f32_e32 v77, v25, v81
	v_and_b32_e32 v79, 0xffff0000, v86
	v_fmac_f32_e32 v130, v77, v92
	v_fmac_f32_e32 v129, v77, v93
	v_fmac_f32_e32 v128, v77, v94
	v_fmac_f32_e32 v124, v77, v95
	v_fmac_f32_e32 v123, v77, v96
	v_fmac_f32_e32 v122, v77, v97
	v_fmac_f32_e32 v119, v77, v98
	v_fmac_f32_e32 v107, v77, v99
	v_mul_f32_e32 v77, v25, v79
	v_fmac_f32_e32 v149, v77, v92
	v_fmac_f32_e32 v148, v77, v93
	v_fmac_f32_e32 v147, v77, v94
	v_fmac_f32_e32 v145, v77, v95
	v_fmac_f32_e32 v143, v77, v96
	v_fmac_f32_e32 v141, v77, v97
	v_fmac_f32_e32 v139, v77, v98
	v_fmac_f32_e32 v137, v77, v99
	v_and_b32_e32 v77, 0xffff0000, v84
	v_mul_f32_e32 v84, v25, v77
	v_fmac_f32_e32 v135, v84, v92
	v_fmac_f32_e32 v133, v84, v93
	v_fmac_f32_e32 v131, v84, v94
	v_fmac_f32_e32 v127, v84, v95
	v_fmac_f32_e32 v126, v84, v96
	v_fmac_f32_e32 v125, v84, v97
	v_fmac_f32_e32 v121, v84, v98
	v_fmac_f32_e32 v120, v84, v99
	ds_read_b128 v[92:95], v116 offset:16448
	ds_read_b128 v[96:99], v116 offset:16464
	v_lshlrev_b32_e32 v90, 16, v91
	v_mul_f32_e32 v84, v26, v90
	v_lshlrev_b32_e32 v88, 16, v89
	s_waitcnt lgkmcnt(1)
	v_fmac_f32_e32 v146, v84, v92
	v_fmac_f32_e32 v144, v84, v93
	v_fmac_f32_e32 v142, v84, v94
	v_fmac_f32_e32 v140, v84, v95
	s_waitcnt lgkmcnt(0)
	v_fmac_f32_e32 v138, v84, v96
	v_fmac_f32_e32 v136, v84, v97
	v_fmac_f32_e32 v134, v84, v98
	v_fmac_f32_e32 v132, v84, v99
	v_mul_f32_e32 v84, v26, v88
	v_lshlrev_b32_e32 v86, 16, v87
	v_fmac_f32_e32 v130, v84, v92
	v_fmac_f32_e32 v129, v84, v93
	v_fmac_f32_e32 v128, v84, v94
	v_fmac_f32_e32 v124, v84, v95
	v_fmac_f32_e32 v123, v84, v96
	v_fmac_f32_e32 v122, v84, v97
	v_fmac_f32_e32 v119, v84, v98
	v_fmac_f32_e32 v107, v84, v99
	v_mul_f32_e32 v84, v26, v86
	v_fmac_f32_e32 v149, v84, v92
	v_fmac_f32_e32 v148, v84, v93
	v_fmac_f32_e32 v147, v84, v94
	v_fmac_f32_e32 v145, v84, v95
	v_fmac_f32_e32 v143, v84, v96
	v_fmac_f32_e32 v141, v84, v97
	v_fmac_f32_e32 v139, v84, v98
	v_fmac_f32_e32 v137, v84, v99
	v_lshlrev_b32_e32 v84, 16, v85
	v_mul_f32_e32 v103, v26, v84
	v_fmac_f32_e32 v135, v103, v92
	v_fmac_f32_e32 v133, v103, v93
	v_fmac_f32_e32 v131, v103, v94
	v_fmac_f32_e32 v127, v103, v95
	v_fmac_f32_e32 v126, v103, v96
	v_fmac_f32_e32 v125, v103, v97
	v_fmac_f32_e32 v121, v103, v98
	v_fmac_f32_e32 v120, v103, v99
	ds_read_b128 v[92:95], v116 offset:16480
	ds_read_b128 v[96:99], v116 offset:16496
	v_and_b32_e32 v91, 0xffff0000, v91
	v_mul_f32_e32 v103, v27, v91
	v_and_b32_e32 v89, 0xffff0000, v89
	s_waitcnt lgkmcnt(1)
	v_fmac_f32_e32 v146, v103, v92
	v_fmac_f32_e32 v144, v103, v93
	v_fmac_f32_e32 v142, v103, v94
	v_fmac_f32_e32 v140, v103, v95
	s_waitcnt lgkmcnt(0)
; #define LAS __attribute__((address_space(3)))
; __device__ __forceinline__ float bf_lo(unsigned w) { return __uint_as_float(w << 16); }
; __device__ __forceinline__ float bf_hi(unsigned w) { return __uint_as_float(w & 0xffff0000u); }
; __device__ __forceinline__ void route_rows(Frame& F, const bf16* xin, const float* g, const float* shift, const float* scale, const float* w_router, const float* b_router,
;                                            unsigned char* XS, float* wl, int* posi, gu32* cnt) {
;     ...
; #pragma unroll
;             for (int j = 0; j < 4; ++j)
; #pragma unroll
;                 for (int i = 0; i < 4; ++i) { const LAS f32x4* wq = (const LAS f32x4*)(wr + (size_t)(4 * lane + 256 * j + i) * 8); const f32x4 wa = wq[0], wb = wq[1]; const float gsv = gs[j][i];
; #pragma unroll
;                     for (int r = 0; r < 4; ++r) { const unsigned wd = (i < 2) ? xb[r][j].x : xb[r][j].y; const float xv = (i & 1) ? bf_hi(wd) : bf_lo(wd), xt = xv * gsv;
;                         ss[r] += xv * xv;
;                         lg[8 * r + 0] += xt * wa.x; lg[8 * r + 1] += xt * wa.y; lg[8 * r + 2] += xt * wa.z; lg[8 * r + 3] += xt * wa.w; lg[8 * r + 4] += xt * wb.x; lg[8 * r + 5] += xt * wb.y; lg[8 * r + 6] += xt * wb.z; lg[8 * r + 7] += xt * wb.w; } }
	v_fmac_f32_e32 v138, v103, v96
	v_fmac_f32_e32 v136, v103, v97
	v_fmac_f32_e32 v134, v103, v98
	v_fmac_f32_e32 v132, v103, v99
	v_mul_f32_e32 v103, v27, v89
	v_and_b32_e32 v87, 0xffff0000, v87
	ds_read_b128 v[152:155], v116 offset:24576
	ds_read_b128 v[156:159], v116 offset:24592
	v_fmac_f32_e32 v130, v103, v92
	v_fmac_f32_e32 v129, v103, v93
	v_fmac_f32_e32 v128, v103, v94
	v_fmac_f32_e32 v124, v103, v95
	v_fmac_f32_e32 v123, v103, v96
	v_fmac_f32_e32 v122, v103, v97
	v_fmac_f32_e32 v119, v103, v98
	v_fmac_f32_e32 v107, v103, v99
	v_mul_f32_e32 v103, v27, v87
	v_and_b32_e32 v85, 0xffff0000, v85
	v_fmac_f32_e32 v149, v103, v92
	v_fmac_f32_e32 v148, v103, v93
	v_fmac_f32_e32 v147, v103, v94
	v_fmac_f32_e32 v145, v103, v95
	v_fmac_f32_e32 v143, v103, v96
	v_fmac_f32_e32 v141, v103, v97
	v_fmac_f32_e32 v139, v103, v98
	v_fmac_f32_e32 v137, v103, v99
	v_mul_f32_e32 v103, v27, v85
	v_mul_f32_e32 v101, v37, v37
	v_fmac_f32_e32 v121, v103, v98
	v_lshlrev_b32_e32 v98, 16, v58
	v_fmac_f32_e32 v101, v36, v36
	v_fmac_f32_e32 v135, v103, v92
	v_fmac_f32_e32 v126, v103, v96
	v_mul_f32_e32 v92, v16, v98
	v_lshlrev_b32_e32 v96, 16, v62
	v_fmac_f32_e32 v101, v50, v50
	v_fmac_f32_e32 v131, v103, v94
	s_waitcnt lgkmcnt(1)
	v_fmac_f32_e32 v146, v92, v152
	v_fmac_f32_e32 v144, v92, v153
	v_fmac_f32_e32 v142, v92, v154
	v_fmac_f32_e32 v140, v92, v155
	s_waitcnt lgkmcnt(0)
	v_fmac_f32_e32 v138, v92, v156
	v_fmac_f32_e32 v136, v92, v157
	v_fmac_f32_e32 v134, v92, v158
	v_fmac_f32_e32 v132, v92, v159
	v_mul_f32_e32 v92, v16, v96
	v_lshlrev_b32_e32 v94, 16, v54
	v_mul_f32_e32 v102, v31, v31
	v_fmac_f32_e32 v101, v51, v51
	v_fmac_f32_e32 v130, v92, v152
	v_fmac_f32_e32 v129, v92, v153
	v_fmac_f32_e32 v128, v92, v154
	v_fmac_f32_e32 v124, v92, v155
	v_fmac_f32_e32 v123, v92, v156
	v_fmac_f32_e32 v122, v92, v157
	v_fmac_f32_e32 v119, v92, v158
	v_fmac_f32_e32 v107, v92, v159
	v_mul_f32_e32 v92, v16, v94
	v_fmac_f32_e32 v102, v30, v30
	v_fmac_f32_e32 v101, v66, v66
	v_fmac_f32_e32 v149, v92, v152
	v_fmac_f32_e32 v148, v92, v153
	v_fmac_f32_e32 v147, v92, v154
	v_fmac_f32_e32 v145, v92, v155
	v_fmac_f32_e32 v143, v92, v156
	v_fmac_f32_e32 v141, v92, v157
	v_fmac_f32_e32 v139, v92, v158
	v_fmac_f32_e32 v137, v92, v159
	s_waitcnt vmcnt(0)
	v_lshlrev_b32_e32 v92, 16, v56
	v_fmac_f32_e32 v102, v46, v46
	v_fmac_f32_e32 v101, v67, v67
	v_fmac_f32_e32 v133, v103, v93
	v_fmac_f32_e32 v127, v103, v95
	v_fmac_f32_e32 v125, v103, v97
	v_fmac_f32_e32 v120, v103, v99
	v_mul_f32_e32 v93, v16, v92
	v_fmac_f32_e32 v102, v47, v47
	v_fmac_f32_e32 v101, v74, v74
	v_fmac_f32_e32 v135, v93, v152
	v_fmac_f32_e32 v133, v93, v153
	v_fmac_f32_e32 v131, v93, v154
	v_fmac_f32_e32 v127, v93, v155
	v_fmac_f32_e32 v126, v93, v156
	v_fmac_f32_e32 v125, v93, v157
	v_fmac_f32_e32 v121, v93, v158
	v_fmac_f32_e32 v120, v93, v159
	ds_read_b128 v[152:155], v116 offset:24608
	ds_read_b128 v[156:159], v116 offset:24624
	v_mul_f32_e32 v100, v29, v29
	v_fmac_f32_e32 v102, v64, v64
	v_fmac_f32_e32 v101, v75, v75
	v_fmac_f32_e32 v100, v28, v28
	v_fmac_f32_e32 v102, v65, v65
	v_fmac_f32_e32 v101, v82, v82
	v_fmac_f32_e32 v100, v44, v44
	v_fmac_f32_e32 v102, v72, v72
	v_fmac_f32_e32 v101, v83, v83
	v_and_b32_e32 v99, 0xffff0000, v58
	v_and_b32_e32 v95, 0xffff0000, v54
	v_mul_f32_e32 v150, v23, v23
	v_fmac_f32_e32 v100, v45, v45
	v_fmac_f32_e32 v102, v73, v73
	v_fmac_f32_e32 v101, v90, v90
	v_mul_f32_e32 v58, v17, v99
	v_and_b32_e32 v97, 0xffff0000, v62
	v_mul_f32_e32 v54, v17, v95
	v_and_b32_e32 v93, 0xffff0000, v56
	v_fmac_f32_e32 v150, v22, v22
	v_fmac_f32_e32 v100, v60, v60
	v_fmac_f32_e32 v102, v80, v80
	v_fmac_f32_e32 v101, v91, v91
	s_waitcnt lgkmcnt(1)
	v_fmac_f32_e32 v146, v58, v152
	v_fmac_f32_e32 v144, v58, v153
	v_fmac_f32_e32 v142, v58, v154
	v_fmac_f32_e32 v140, v58, v155
	s_waitcnt lgkmcnt(0)
	v_fmac_f32_e32 v138, v58, v156
	v_fmac_f32_e32 v136, v58, v157
	v_fmac_f32_e32 v134, v58, v158
	v_fmac_f32_e32 v132, v58, v159
	v_mul_f32_e32 v58, v17, v97
	v_fmac_f32_e32 v149, v54, v152
	v_fmac_f32_e32 v148, v54, v153
	v_fmac_f32_e32 v147, v54, v154
	v_fmac_f32_e32 v145, v54, v155
	v_fmac_f32_e32 v143, v54, v156
	v_fmac_f32_e32 v141, v54, v157
	v_fmac_f32_e32 v139, v54, v158
	v_fmac_f32_e32 v137, v54, v159
	v_mul_f32_e32 v54, v17, v93
	v_fmac_f32_e32 v150, v38, v38
	v_fmac_f32_e32 v100, v61, v61
	v_fmac_f32_e32 v102, v81, v81
	v_fmac_f32_e32 v101, v98, v98
	v_fmac_f32_e32 v130, v58, v152
	v_fmac_f32_e32 v129, v58, v153
	v_fmac_f32_e32 v128, v58, v154
	v_fmac_f32_e32 v124, v58, v155
	v_fmac_f32_e32 v123, v58, v156
	v_fmac_f32_e32 v122, v58, v157
	v_fmac_f32_e32 v119, v58, v158
	v_fmac_f32_e32 v107, v58, v159
	v_fmac_f32_e32 v135, v54, v152
	v_fmac_f32_e32 v133, v54, v153
	v_fmac_f32_e32 v131, v54, v154
	v_fmac_f32_e32 v127, v54, v155
	v_fmac_f32_e32 v126, v54, v156
	v_fmac_f32_e32 v125, v54, v157
	v_fmac_f32_e32 v121, v54, v158
	v_fmac_f32_e32 v120, v54, v159
	ds_read_b128 v[152:155], v116 offset:24640
	ds_read_b128 v[156:159], v116 offset:24656
	ds_read_b128 v[160:163], v116 offset:24672
	ds_read_b128 v[164:167], v116 offset:24688
	v_fmac_f32_e32 v150, v39, v39
	v_fmac_f32_e32 v100, v70, v70
	v_fmac_f32_e32 v102, v88, v88
	v_fmac_f32_e32 v101, v99, v99
	v_pk_mul_f32 v[104:105], v[108:109], v[108:109]
	v_fmac_f32_e32 v150, v52, v52
	v_fmac_f32_e32 v100, v71, v71
	v_fmac_f32_e32 v102, v89, v89
	v_add_f32_e32 v56, v105, v101
	v_and_b32_e32 v62, 0xffff0000, v63
	v_fmac_f32_e32 v150, v53, v53
	v_fmac_f32_e32 v100, v78, v78
	v_fmac_f32_e32 v102, v96, v96
	v_mul_f32_e32 v54, v18, v109
	v_add_f32_e32 v56, v104, v56
	v_lshlrev_b32_e32 v105, 16, v63
	v_mov_b32_e32 v104, v62
	v_fmac_f32_e32 v150, v68, v68
	v_fmac_f32_e32 v100, v79, v79
	v_fmac_f32_e32 v102, v97, v97
	s_waitcnt lgkmcnt(3)
; #define LAS __attribute__((address_space(3)))
; __device__ __forceinline__ float bf_lo(unsigned w) { return __uint_as_float(w << 16); }
; __device__ __forceinline__ float bf_hi(unsigned w) { return __uint_as_float(w & 0xffff0000u); }
; #define RR_STEP(ARR, N, MSK) do { const bool up_ = (pg8::pg8_lane_id() & (MSK)) != 0; _Pragma("unroll") for (int k_ = 0; k_ < (N) / 2; ++k_) { const float lo_ = ARR[k_], hi_ = ARR[k_ + (N) / 2]; \
;         const float snd_ = up_ ? lo_ : hi_, kp_ = up_ ? hi_ : lo_; ARR[k_] = kp_ + rr_shx(snd_, (MSK)); } } while (0)
; __device__ __forceinline__ void route_rows(Frame& F, const bf16* xin, const float* g, const float* shift, const float* scale, const float* w_router, const float* b_router,
;                                            unsigned char* XS, float* wl, int* posi, gu32* cnt) {
;     ...
; #pragma unroll
;             for (int j = 0; j < 4; ++j)
; #pragma unroll
;                 for (int i = 0; i < 4; ++i) { const LAS f32x4* wq = (const LAS f32x4*)(wr + (size_t)(4 * lane + 256 * j + i) * 8); const f32x4 wa = wq[0], wb = wq[1]; const float gsv = gs[j][i];
; #pragma unroll
;                     for (int r = 0; r < 4; ++r) { const unsigned wd = (i < 2) ? xb[r][j].x : xb[r][j].y; const float xv = (i & 1) ? bf_hi(wd) : bf_lo(wd), xt = xv * gsv;
;                         ss[r] += xv * xv;
;                         lg[8 * r + 0] += xt * wa.x; lg[8 * r + 1] += xt * wa.y; lg[8 * r + 2] += xt * wa.z; lg[8 * r + 3] += xt * wa.w; lg[8 * r + 4] += xt * wb.x; lg[8 * r + 5] += xt * wb.y; lg[8 * r + 6] += xt * wb.z; lg[8 * r + 7] += xt * wb.w; } }
;             RR_STEP(lg, 32, 32); RR_STEP(lg, 16, 16); RR_STEP(lg, 8, 8); RR_STEP(lg, 4, 4); RR_STEP(lg, 2, 2);
	v_fmac_f32_e32 v146, v54, v152
	v_fmac_f32_e32 v144, v54, v153
	v_fmac_f32_e32 v142, v54, v154
	v_fmac_f32_e32 v140, v54, v155
	s_waitcnt lgkmcnt(2)
	v_fmac_f32_e32 v138, v54, v156
	v_fmac_f32_e32 v136, v54, v157
	v_fmac_f32_e32 v134, v54, v158
	v_fmac_f32_e32 v132, v54, v159
	v_mul_f32_e32 v54, v19, v106
	v_pk_mul_f32 v[168:169], v[104:105], v[104:105]
	v_fmac_f32_e32 v150, v69, v69
	v_fmac_f32_e32 v100, v86, v86
	s_waitcnt lgkmcnt(1)
	v_fmac_f32_e32 v146, v54, v160
	v_fmac_f32_e32 v144, v54, v161
	v_fmac_f32_e32 v142, v54, v162
	v_fmac_f32_e32 v140, v54, v163
	s_waitcnt lgkmcnt(0)
	v_fmac_f32_e32 v138, v54, v164
	v_fmac_f32_e32 v136, v54, v165
	v_fmac_f32_e32 v134, v54, v166
	v_fmac_f32_e32 v132, v54, v167
	v_mul_f32_e32 v54, v18, v105
	v_add_f32_e32 v58, v169, v102
	v_fmac_f32_e32 v150, v76, v76
	v_fmac_f32_e32 v100, v87, v87
	v_fmac_f32_e32 v130, v54, v152
	v_fmac_f32_e32 v129, v54, v153
	v_fmac_f32_e32 v128, v54, v154
	v_fmac_f32_e32 v124, v54, v155
	v_fmac_f32_e32 v123, v54, v156
	v_fmac_f32_e32 v122, v54, v157
	v_fmac_f32_e32 v119, v54, v158
	v_fmac_f32_e32 v107, v54, v159
	v_mul_f32_e32 v54, v19, v62
	v_add_f32_e32 v104, v168, v58
	v_and_b32_e32 v58, 0xffff0000, v55
	v_lshlrev_b32_e32 v103, 16, v55
	v_fmac_f32_e32 v150, v77, v77
	v_fmac_f32_e32 v100, v94, v94
	v_fmac_f32_e32 v130, v54, v160
	v_fmac_f32_e32 v129, v54, v161
	v_fmac_f32_e32 v128, v54, v162
	v_fmac_f32_e32 v124, v54, v163
	v_fmac_f32_e32 v123, v54, v164
	v_fmac_f32_e32 v122, v54, v165
	v_fmac_f32_e32 v119, v54, v166
	v_fmac_f32_e32 v107, v54, v167
	v_mov_b32_e32 v102, v58
	v_mul_f32_e32 v54, v18, v103
	v_fmac_f32_e32 v150, v84, v84
	v_fmac_f32_e32 v100, v95, v95
	v_pk_mul_f32 v[168:169], v[102:103], v[102:103]
	v_fmac_f32_e32 v149, v54, v152
	v_fmac_f32_e32 v148, v54, v153
	v_fmac_f32_e32 v147, v54, v154
	v_fmac_f32_e32 v145, v54, v155
	v_fmac_f32_e32 v143, v54, v156
	v_fmac_f32_e32 v141, v54, v157
	v_fmac_f32_e32 v139, v54, v158
	v_fmac_f32_e32 v137, v54, v159
	v_mul_f32_e32 v54, v19, v58
	v_fmac_f32_e32 v150, v85, v85
	v_add_f32_e32 v100, v169, v100
	v_fmac_f32_e32 v149, v54, v160
	v_fmac_f32_e32 v148, v54, v161
	v_fmac_f32_e32 v147, v54, v162
	v_fmac_f32_e32 v145, v54, v163
	v_fmac_f32_e32 v143, v54, v164
	v_fmac_f32_e32 v141, v54, v165
	v_fmac_f32_e32 v139, v54, v166
	v_fmac_f32_e32 v137, v54, v167
	v_and_b32_e32 v54, 0xffff0000, v57
	v_fmac_f32_e32 v150, v92, v92
	v_add_f32_e32 v108, v168, v100
	v_lshlrev_b32_e32 v101, 16, v57
	v_mov_b32_e32 v100, v54
	v_fmac_f32_e32 v150, v93, v93
	v_pk_mul_f32 v[168:169], v[100:101], v[100:101]
	v_mul_f32_e32 v102, v18, v101
	v_add_f32_e32 v100, v169, v150
	v_add_f32_e32 v150, v168, v100
	v_mbcnt_lo_u32_b32 v100, -1, 0
	v_mbcnt_hi_u32_b32 v100, -1, v100
	v_mbcnt_lo_u32_b32 v151, -1, 0
	v_mbcnt_hi_u32_b32 v151, -1, v151
	v_fmac_f32_e32 v135, v102, v152
	v_and_b32_e32 v100, 32, v100
	v_cmp_eq_u32_e32 vcc, 0, v100
	v_lshlrev_b32_e32 v151, 2, v151
	v_xor_b32_e32 v151, 0x80, v151
	v_cndmask_b32_e32 v100, v146, v149, vcc
	ds_bpermute_b32 v100, v151, v100
	v_fmac_f32_e32 v133, v102, v153
	v_fmac_f32_e32 v131, v102, v154
	v_fmac_f32_e32 v127, v102, v155
	v_fmac_f32_e32 v126, v102, v156
	v_fmac_f32_e32 v125, v102, v157
	v_fmac_f32_e32 v121, v102, v158
	v_fmac_f32_e32 v120, v102, v159
	v_mul_f32_e32 v102, v19, v54
	v_fmac_f32_e32 v135, v102, v160
	v_fmac_f32_e32 v133, v102, v161
	v_fmac_f32_e32 v131, v102, v162
	v_fmac_f32_e32 v127, v102, v163
	v_fmac_f32_e32 v126, v102, v164
	v_fmac_f32_e32 v125, v102, v165
	v_fmac_f32_e32 v121, v102, v166
	v_fmac_f32_e32 v120, v102, v167
	v_cndmask_b32_e32 v102, v149, v146, vcc
	v_mbcnt_lo_u32_b32 v146, -1, 0
	v_mbcnt_hi_u32_b32 v146, -1, v146
	s_waitcnt lgkmcnt(0)
	v_add_f32_e32 v100, v102, v100
	v_lshlrev_b32_e32 v146, 2, v146
	v_cndmask_b32_e32 v102, v144, v148, vcc
	v_xor_b32_e32 v146, 0x80, v146
	ds_bpermute_b32 v102, v146, v102
	v_cndmask_b32_e32 v144, v148, v144, vcc
	v_mbcnt_lo_u32_b32 v148, -1, 0
	v_mbcnt_hi_u32_b32 v148, -1, v148
	v_cndmask_b32_e32 v146, v142, v147, vcc
	v_lshlrev_b32_e32 v148, 2, v148
	v_xor_b32_e32 v148, 0x80, v148
	ds_bpermute_b32 v146, v148, v146
	v_mbcnt_lo_u32_b32 v149, -1, 0
	v_mbcnt_hi_u32_b32 v149, -1, v149
	s_waitcnt lgkmcnt(1)
	v_add_f32_e32 v102, v144, v102
	v_cndmask_b32_e32 v144, v138, v143, vcc
	v_cndmask_b32_e32 v138, v143, v138, vcc
	v_mbcnt_lo_u32_b32 v143, -1, 0
	v_mbcnt_hi_u32_b32 v143, -1, v143
	v_cndmask_b32_e32 v148, v140, v145, vcc
	v_cndmask_b32_e32 v140, v145, v140, vcc
	v_lshlrev_b32_e32 v143, 2, v143
	v_mbcnt_lo_u32_b32 v145, -1, 0
	v_mbcnt_hi_u32_b32 v145, -1, v145
	v_xor_b32_e32 v143, 0x80, v143
	v_lshlrev_b32_e32 v145, 2, v145
	v_cndmask_b32_e32 v142, v147, v142, vcc
	ds_bpermute_b32 v143, v143, v144
	v_cndmask_b32_e32 v144, v136, v141, vcc
	v_xor_b32_e32 v145, 0x80, v145
	s_waitcnt lgkmcnt(1)
	v_add_f32_e32 v142, v142, v146
	ds_bpermute_b32 v144, v145, v144
	v_cndmask_b32_e32 v145, v134, v139, vcc
	v_mbcnt_lo_u32_b32 v146, -1, 0
	v_mbcnt_hi_u32_b32 v146, -1, v146
	v_cndmask_b32_e32 v134, v139, v134, vcc
	v_cndmask_b32_e32 v139, v132, v137, vcc
	v_cndmask_b32_e32 v132, v137, v132, vcc
	v_mbcnt_lo_u32_b32 v137, -1, 0
	v_mbcnt_hi_u32_b32 v137, -1, v137
	v_cndmask_b32_e32 v136, v141, v136, vcc
	v_lshlrev_b32_e32 v137, 2, v137
	v_mbcnt_lo_u32_b32 v141, -1, 0
	v_mbcnt_hi_u32_b32 v141, -1, v141
	v_xor_b32_e32 v137, 0x80, v137
	v_lshlrev_b32_e32 v141, 2, v141
	ds_bpermute_b32 v137, v137, v139
	v_cndmask_b32_e32 v139, v130, v135, vcc
	v_xor_b32_e32 v141, 0x80, v141
	s_waitcnt lgkmcnt(2)
; #define RR_STEP(ARR, N, MSK) do { const bool up_ = (pg8::pg8_lane_id() & (MSK)) != 0; _Pragma("unroll") for (int k_ = 0; k_ < (N) / 2; ++k_) { const float lo_ = ARR[k_], hi_ = ARR[k_ + (N) / 2]; \
;         const float snd_ = up_ ? lo_ : hi_, kp_ = up_ ? hi_ : lo_; ARR[k_] = kp_ + rr_shx(snd_, (MSK)); } } while (0)
; __device__ __forceinline__ void route_rows(Frame& F, const bf16* xin, const float* g, const float* shift, const float* scale, const float* w_router, const float* b_router,
;                                            unsigned char* XS, float* wl, int* posi, gu32* cnt) {
;     ...
;             RR_STEP(lg, 32, 32); RR_STEP(lg, 16, 16); RR_STEP(lg, 8, 8); RR_STEP(lg, 4, 4); RR_STEP(lg, 2, 2);
	v_add_f32_e32 v138, v138, v143
	ds_bpermute_b32 v139, v141, v139
	v_cndmask_b32_e32 v141, v129, v133, vcc
	v_mbcnt_lo_u32_b32 v143, -1, 0
	v_mbcnt_hi_u32_b32 v143, -1, v143
	v_cndmask_b32_e32 v129, v133, v129, vcc
	v_cndmask_b32_e32 v133, v128, v131, vcc
	v_cndmask_b32_e32 v128, v131, v128, vcc
	v_mbcnt_lo_u32_b32 v131, -1, 0
	v_mbcnt_hi_u32_b32 v131, -1, v131
	v_cndmask_b32_e32 v130, v135, v130, vcc
	v_lshlrev_b32_e32 v131, 2, v131
	v_mbcnt_lo_u32_b32 v135, -1, 0
	v_mbcnt_hi_u32_b32 v135, -1, v135
	v_xor_b32_e32 v131, 0x80, v131
	v_lshlrev_b32_e32 v135, 2, v135
	ds_bpermute_b32 v131, v131, v133
	v_cndmask_b32_e32 v133, v124, v127, vcc
	v_xor_b32_e32 v135, 0x80, v135
	s_waitcnt lgkmcnt(2)
	v_add_f32_e32 v132, v132, v137
	ds_bpermute_b32 v133, v135, v133
	v_cndmask_b32_e32 v135, v123, v126, vcc
	v_mbcnt_lo_u32_b32 v137, -1, 0
	v_mbcnt_hi_u32_b32 v137, -1, v137
	v_cndmask_b32_e32 v123, v126, v123, vcc
	v_cndmask_b32_e32 v126, v122, v125, vcc
	v_cndmask_b32_e32 v122, v125, v122, vcc
	v_mbcnt_lo_u32_b32 v125, -1, 0
	v_mbcnt_hi_u32_b32 v125, -1, v125
	v_cndmask_b32_e32 v124, v127, v124, vcc
	v_lshlrev_b32_e32 v125, 2, v125
	v_mbcnt_lo_u32_b32 v127, -1, 0
	v_mbcnt_hi_u32_b32 v127, -1, v127
	v_lshlrev_b32_e32 v143, 2, v143
	v_xor_b32_e32 v125, 0x80, v125
	v_lshlrev_b32_e32 v127, 2, v127
	v_xor_b32_e32 v143, 0x80, v143
	ds_bpermute_b32 v125, v125, v126
	v_cndmask_b32_e32 v126, v119, v121, vcc
	v_xor_b32_e32 v127, 0x80, v127
	ds_bpermute_b32 v141, v143, v141
	ds_bpermute_b32 v126, v127, v126
	s_waitcnt lgkmcnt(4)
	v_add_f32_e32 v128, v128, v131
	v_cndmask_b32_e32 v127, v107, v120, vcc
	v_mbcnt_lo_u32_b32 v131, -1, 0
	v_mbcnt_hi_u32_b32 v131, -1, v131
	v_cndmask_b32_e32 v107, v120, v107, vcc
	v_mbcnt_lo_u32_b32 v120, -1, 0
	v_mbcnt_hi_u32_b32 v120, -1, v120
	v_cndmask_b32_e32 v119, v121, v119, vcc
	v_and_b32_e32 v120, 16, v120
	v_mbcnt_lo_u32_b32 v121, -1, 0
	v_mbcnt_hi_u32_b32 v121, -1, v121
	v_add_f32_e32 v130, v130, v139
	s_waitcnt lgkmcnt(2)
	v_add_f32_e32 v122, v122, v125
	v_cmp_eq_u32_e64 s[4:5], 0, v120
	v_lshlrev_b32_e32 v121, 2, v121
	v_mbcnt_lo_u32_b32 v125, -1, 0
	v_mbcnt_hi_u32_b32 v125, -1, v125
	s_waitcnt lgkmcnt(1)
	v_add_f32_e32 v129, v129, v141
	s_waitcnt lgkmcnt(0)
	v_add_f32_e32 v119, v119, v126
	v_cndmask_b32_e64 v120, v100, v130, s[4:5]
	v_xor_b32_e32 v121, 64, v121
	v_lshlrev_b32_e32 v125, 2, v125
	v_mbcnt_lo_u32_b32 v126, -1, 0
	v_mbcnt_hi_u32_b32 v126, -1, v126
	ds_bpermute_b32 v120, v121, v120
	v_cndmask_b32_e64 v121, v102, v129, s[4:5]
	v_xor_b32_e32 v125, 64, v125
	v_lshlrev_b32_e32 v126, 2, v126
	v_lshlrev_b32_e32 v149, 2, v149
	ds_bpermute_b32 v121, v125, v121
	v_cndmask_b32_e64 v125, v142, v128, s[4:5]
	v_xor_b32_e32 v126, 64, v126
	v_xor_b32_e32 v149, 0x80, v149
	v_lshlrev_b32_e32 v137, 2, v137
	v_lshlrev_b32_e32 v131, 2, v131
	ds_bpermute_b32 v125, v126, v125
	ds_bpermute_b32 v148, v149, v148
	v_xor_b32_e32 v137, 0x80, v137
	v_xor_b32_e32 v131, 0x80, v131
	ds_bpermute_b32 v135, v137, v135
	ds_bpermute_b32 v127, v131, v127
	v_cndmask_b32_e64 v100, v130, v100, s[4:5]
	s_waitcnt lgkmcnt(5)
	v_add_f32_e32 v100, v100, v120
	v_cndmask_b32_e64 v120, v128, v142, s[4:5]
	s_waitcnt lgkmcnt(3)
	v_add_f32_e32 v120, v120, v125
	v_mbcnt_lo_u32_b32 v125, -1, 0
	v_mbcnt_hi_u32_b32 v125, -1, v125
	s_waitcnt lgkmcnt(2)
	v_add_f32_e32 v140, v140, v148
	v_add_f32_e32 v124, v124, v133
	v_cndmask_b32_e64 v102, v129, v102, s[4:5]
	v_lshlrev_b32_e32 v125, 2, v125
	v_mbcnt_lo_u32_b32 v126, -1, 0
	v_mbcnt_hi_u32_b32 v126, -1, v126
	s_waitcnt lgkmcnt(1)
	v_add_f32_e32 v123, v123, v135
	s_waitcnt lgkmcnt(0)
	v_add_f32_e32 v107, v107, v127
	v_add_f32_e32 v102, v102, v121
	v_cndmask_b32_e64 v121, v140, v124, s[4:5]
	v_xor_b32_e32 v125, 64, v125
	v_lshlrev_b32_e32 v126, 2, v126
	v_mbcnt_lo_u32_b32 v127, -1, 0
	v_mbcnt_hi_u32_b32 v127, -1, v127
	v_lshlrev_b32_e32 v146, 2, v146
	v_add_f32_e32 v136, v136, v144
	ds_bpermute_b32 v121, v125, v121
	v_cndmask_b32_e64 v125, v138, v123, s[4:5]
	v_xor_b32_e32 v126, 64, v126
	v_lshlrev_b32_e32 v127, 2, v127
	v_xor_b32_e32 v146, 0x80, v146
	ds_bpermute_b32 v125, v126, v125
	v_cndmask_b32_e64 v126, v136, v122, s[4:5]
	v_xor_b32_e32 v127, 64, v127
	ds_bpermute_b32 v145, v146, v145
	ds_bpermute_b32 v126, v127, v126
	v_cndmask_b32_e64 v123, v123, v138, s[4:5]
	s_waitcnt lgkmcnt(2)
	v_add_f32_e32 v123, v123, v125
	v_cndmask_b32_e64 v122, v122, v136, s[4:5]
	v_mbcnt_lo_u32_b32 v125, -1, 0
	v_mbcnt_hi_u32_b32 v125, -1, v125
	s_waitcnt lgkmcnt(1)
	v_add_f32_e32 v134, v134, v145
	v_cndmask_b32_e64 v124, v124, v140, s[4:5]
	s_waitcnt lgkmcnt(0)
	v_add_f32_e32 v122, v122, v126
	v_lshlrev_b32_e32 v125, 2, v125
	v_mbcnt_lo_u32_b32 v126, -1, 0
	v_mbcnt_hi_u32_b32 v126, -1, v126
	v_add_f32_e32 v121, v124, v121
	v_cndmask_b32_e64 v124, v134, v119, s[4:5]
	v_xor_b32_e32 v125, 64, v125
	v_lshlrev_b32_e32 v126, 2, v126
	ds_bpermute_b32 v124, v125, v124
	v_cndmask_b32_e64 v125, v132, v107, s[4:5]
	v_xor_b32_e32 v126, 64, v126
	ds_bpermute_b32 v125, v126, v125
	v_mbcnt_lo_u32_b32 v126, -1, 0
	v_mbcnt_hi_u32_b32 v126, -1, v126
	v_mbcnt_lo_u32_b32 v127, -1, 0
	v_mbcnt_hi_u32_b32 v127, -1, v127
	v_cndmask_b32_e64 v119, v119, v134, s[4:5]
	v_and_b32_e32 v126, 8, v126
	v_cmp_eq_u32_e32 vcc, 0, v126
	v_lshlrev_b32_e32 v127, 2, v127
	v_xor_b32_e32 v127, 32, v127
	v_cndmask_b32_e32 v126, v100, v123, vcc
	ds_bpermute_b32 v126, v127, v126
	v_cndmask_b32_e32 v100, v123, v100, vcc
	s_waitcnt lgkmcnt(2)
	v_add_f32_e32 v119, v119, v124
	v_cndmask_b32_e64 v107, v107, v132, s[4:5]
	s_waitcnt lgkmcnt(1)
	v_add_f32_e32 v107, v107, v125
	s_waitcnt lgkmcnt(0)
; __device__ __forceinline__ int pg8_lane_id() { int l; asm volatile("v_mbcnt_lo_u32_b32 %0, -1, 0\n\tv_mbcnt_hi_u32_b32 %0, -1, %0" : "=v"(l)); return l; }
; __device__ __forceinline__ float rr_shx(float v, int m) { return __builtin_bit_cast(float, __builtin_amdgcn_ds_bpermute((pg8::pg8_lane_id() ^ m) << 2, __builtin_bit_cast(int, v))); }
; __device__ __forceinline__ int rr_shxi(int v, int m) { return __builtin_amdgcn_ds_bpermute((pg8::pg8_lane_id() ^ m) << 2, v); }
; #define RR_STEP(ARR, N, MSK) do { const bool up_ = (pg8::pg8_lane_id() & (MSK)) != 0; _Pragma("unroll") for (int k_ = 0; k_ < (N) / 2; ++k_) { const float lo_ = ARR[k_], hi_ = ARR[k_ + (N) / 2]; \
;         const float snd_ = up_ ? lo_ : hi_, kp_ = up_ ? hi_ : lo_; ARR[k_] = kp_ + rr_shx(snd_, (MSK)); } } while (0)
; __device__ __forceinline__ void route_rows(Frame& F, const bf16* xin, const float* g, const float* shift, const float* scale, const float* w_router, const float* b_router,
;                                            unsigned char* XS, float* wl, int* posi, gu32* cnt) {
;     ...
;             RR_STEP(lg, 32, 32); RR_STEP(lg, 16, 16); RR_STEP(lg, 8, 8); RR_STEP(lg, 4, 4); RR_STEP(lg, 2, 2);
;             const float lt = lg[0] + rr_shx(lg[0], 1);
;             RR_STEP(ss, 4, 32); RR_STEP(ss, 2, 16);
;             float sq = ss[0];
; #pragma unroll
;             for (int o = 1; o < 16; o <<= 1) sq += rr_shx(sq, o);
;             const float rstd = rsqrtf(sq * (1.f / D) + RMS_EPS);
;             const int ln = pg8::pg8_lane_id(), e = (ln >> 1) & 7;
;             const float lv = lt * rstd + cbe + b_router[e];
;             float v0 = lv; int i0 = e;
; #pragma unroll
;             for (int o = 2; o < 16; o <<= 1) { const float ov = rr_shx(v0, o); const int oi = rr_shxi(i0, o); const bool t = (ov > v0) || (ov == v0 && oi < i0); v0 = t ? ov : v0; i0 = t ? oi : i0; }
;             float v1 = (e == i0) ? -INFINITY : lv; int i1 = (e == i0) ? 8 : e;
; #pragma unroll
;             for (int o = 2; o < 16; o <<= 1) { const float ov = rr_shx(v1, o); const int oi = rr_shxi(i1, o); const bool t = (ov > v1) || (ov == v1 && oi < i1); v1 = t ? ov : v1; i1 = t ? oi : i1; }
	v_add_f32_e32 v123, v100, v126
	v_cndmask_b32_e32 v100, v102, v122, vcc
	v_cndmask_b32_e32 v122, v122, v102, vcc
	v_mbcnt_lo_u32_b32 v102, -1, 0
	v_mbcnt_hi_u32_b32 v102, -1, v102
	v_and_b32_e32 v63, 16, v63
	v_lshlrev_b32_e32 v102, 2, v102
	v_xor_b32_e32 v102, 32, v102
	ds_bpermute_b32 v124, v102, v100
	v_mbcnt_lo_u32_b32 v102, -1, 0
	v_mbcnt_hi_u32_b32 v102, -1, v102
	v_cndmask_b32_e32 v100, v120, v119, vcc
	v_lshlrev_b32_e32 v102, 2, v102
	v_xor_b32_e32 v102, 32, v102
	ds_bpermute_b32 v125, v102, v100
	v_mbcnt_lo_u32_b32 v102, -1, 0
	v_mbcnt_hi_u32_b32 v102, -1, v102
	v_cndmask_b32_e32 v100, v121, v107, vcc
	v_lshlrev_b32_e32 v102, 2, v102
	v_xor_b32_e32 v102, 32, v102
	ds_bpermute_b32 v126, v102, v100
	v_mbcnt_lo_u32_b32 v127, -1, 0
	v_mbcnt_hi_u32_b32 v127, -1, v127
	v_mbcnt_lo_u32_b32 v128, -1, 0
	v_mbcnt_hi_u32_b32 v128, -1, v128
	v_mbcnt_lo_u32_b32 v129, -1, 0
	v_mbcnt_hi_u32_b32 v129, -1, v129
	v_mbcnt_lo_u32_b32 v130, -1, 0
	v_mbcnt_hi_u32_b32 v130, -1, v130
	v_mbcnt_lo_u32_b32 v131, -1, 0
	v_mbcnt_hi_u32_b32 v131, -1, v131
	v_mbcnt_lo_u32_b32 v132, -1, 0
	v_mbcnt_hi_u32_b32 v132, -1, v132
	v_mbcnt_lo_u32_b32 v133, -1, 0
	v_mbcnt_hi_u32_b32 v133, -1, v133
	v_mbcnt_lo_u32_b32 v134, -1, 0
	v_mbcnt_hi_u32_b32 v134, -1, v134
	v_mbcnt_lo_u32_b32 v135, -1, 0
	v_mbcnt_hi_u32_b32 v135, -1, v135
	v_mbcnt_lo_u32_b32 v136, -1, 0
	v_mbcnt_hi_u32_b32 v136, -1, v136
	v_mbcnt_lo_u32_b32 v137, -1, 0
	v_mbcnt_hi_u32_b32 v137, -1, v137
	v_mbcnt_lo_u32_b32 v138, -1, 0
	v_mbcnt_hi_u32_b32 v138, -1, v138
	v_mbcnt_lo_u32_b32 v139, -1, 0
	v_mbcnt_hi_u32_b32 v139, -1, v139
	v_mbcnt_lo_u32_b32 v140, -1, 0
	v_mbcnt_hi_u32_b32 v140, -1, v140
	v_mbcnt_lo_u32_b32 v141, -1, 0
	v_mbcnt_hi_u32_b32 v141, -1, v141
	v_mbcnt_lo_u32_b32 v100, -1, 0
	v_mbcnt_hi_u32_b32 v100, -1, v100
	s_waitcnt lgkmcnt(2)
	v_add_f32_e32 v122, v122, v124
	v_bfe_u32 v102, v100, 1, 3
	v_lshlrev_b32_e32 v142, 2, v102
	global_load_dword v142, v142, s[70:71]
	v_cndmask_b32_e32 v119, v119, v120, vcc
	v_and_b32_e32 v124, 32, v133
	s_waitcnt lgkmcnt(1)
	v_add_f32_e32 v119, v119, v125
	v_cndmask_b32_e32 v107, v107, v121, vcc
	v_cmp_eq_u32_e64 s[4:5], 0, v124
	v_lshlrev_b32_e32 v125, 2, v134
	s_waitcnt lgkmcnt(0)
	v_add_f32_e32 v107, v107, v126
	v_cndmask_b32_e64 v124, v56, v108, s[4:5]
	v_xor_b32_e32 v125, 0x80, v125
	v_lshlrev_b32_e32 v126, 2, v135
	ds_bpermute_b32 v124, v125, v124
	v_cndmask_b32_e64 v125, v104, v150, s[4:5]
	v_xor_b32_e32 v126, 0x80, v126
	ds_bpermute_b32 v125, v126, v125
	v_and_b32_e32 v120, 4, v127
	v_cmp_eq_u32_e32 vcc, 0, v120
	v_lshlrev_b32_e32 v121, 2, v128
	v_xor_b32_e32 v121, 16, v121
	v_cndmask_b32_e32 v120, v123, v119, vcc
	v_cndmask_b32_e64 v56, v108, v56, s[4:5]
	v_cndmask_b32_e64 v104, v150, v104, s[4:5]
	v_and_b32_e32 v108, 16, v136
	ds_bpermute_b32 v120, v121, v120
	s_waitcnt lgkmcnt(2)
	v_add_f32_e32 v56, v56, v124
	s_waitcnt lgkmcnt(1)
	v_add_f32_e32 v104, v104, v125
	v_cmp_eq_u32_e64 s[4:5], 0, v108
	v_lshlrev_b32_e32 v121, 2, v137
	v_xor_b32_e32 v121, 64, v121
	v_cndmask_b32_e64 v108, v56, v104, s[4:5]
	ds_bpermute_b32 v108, v121, v108
	v_cndmask_b32_e64 v56, v104, v56, s[4:5]
	v_lshlrev_b32_e32 v104, 2, v138
	v_xor_b32_e32 v104, 4, v104
	v_cndmask_b32_e32 v119, v119, v123, vcc
	s_waitcnt lgkmcnt(0)
	v_add_f32_e32 v56, v56, v108
	ds_bpermute_b32 v104, v104, v56
	v_lshlrev_b32_e32 v108, 2, v129
	v_add_f32_e32 v119, v119, v120
	v_cndmask_b32_e32 v120, v122, v107, vcc
	v_xor_b32_e32 v108, 16, v108
	s_waitcnt lgkmcnt(0)
	v_add_f32_e32 v56, v56, v104
	v_lshlrev_b32_e32 v104, 2, v139
	v_xor_b32_e32 v104, 8, v104
	ds_bpermute_b32 v104, v104, v56
	ds_bpermute_b32 v108, v108, v120
	v_cndmask_b32_e32 v107, v107, v122, vcc
	s_mov_b64 s[4:5], -1
	s_waitcnt lgkmcnt(1)
	v_add_f32_e32 v56, v56, v104
	v_lshlrev_b32_e32 v104, 2, v140
	v_xor_b32_e32 v104, 16, v104
	ds_bpermute_b32 v104, v104, v56
	s_waitcnt lgkmcnt(1)
	v_add_f32_e32 v107, v107, v108
	v_and_b32_e32 v108, 2, v130
	v_cmp_eq_u32_e32 vcc, 0, v108
	s_waitcnt lgkmcnt(0)
	v_add_f32_e32 v56, v56, v104
	v_lshlrev_b32_e32 v104, 2, v141
	v_xor_b32_e32 v104, 32, v104
	v_cndmask_b32_e32 v108, v119, v107, vcc
	v_cndmask_b32_e32 v107, v107, v119, vcc
	v_lshlrev_b32_e32 v119, 2, v131
	ds_bpermute_b32 v104, v104, v56
	v_xor_b32_e32 v119, 8, v119
	ds_bpermute_b32 v108, v119, v108
	s_waitcnt lgkmcnt(1)
	v_add_f32_e32 v56, v56, v104
	v_fmamk_f32 v56, v56, 0x3a800000, v111
	s_waitcnt lgkmcnt(0)
	v_add_f32_e32 v108, v107, v108
	v_lshlrev_b32_e32 v107, 2, v132
	v_mul_f32_e32 v104, 0x4b800000, v56
	v_cmp_gt_f32_e32 vcc, s42, v56
	v_xor_b32_e32 v107, 4, v107
	ds_bpermute_b32 v119, v107, v108
	v_cndmask_b32_e32 v56, v56, v104, vcc
	v_rsq_f32_e32 v56, v56
	v_and_b32_e32 v107, 16, v59
	s_waitcnt lgkmcnt(0)
	v_add_f32_e32 v59, v108, v119
	v_mul_f32_e32 v104, 0x45800000, v56
	v_cndmask_b32_e32 v56, v56, v104, vcc
	v_fma_f32 v59, v59, v56, v117
	s_waitcnt vmcnt(0)
	v_add_f32_e32 v119, v142, v59
	v_mbcnt_lo_u32_b32 v59, -1, 0
	v_mbcnt_hi_u32_b32 v59, -1, v59
	s_nop 0
	v_lshlrev_b32_e32 v59, 2, v59
	v_xor_b32_e32 v59, 8, v59
	ds_bpermute_b32 v104, v59, v119
	v_mbcnt_lo_u32_b32 v59, -1, 0
	v_mbcnt_hi_u32_b32 v59, -1, v59
	s_waitcnt lgkmcnt(0)
	v_cmp_nlt_f32_e32 vcc, v119, v104
	v_lshlrev_b32_e32 v59, 2, v59
	v_xor_b32_e32 v59, 8, v59
	ds_bpermute_b32 v108, v59, v102
	v_and_b32_e32 v59, 16, v55
	v_and_b32_e32 v55, 16, v57
	s_and_saveexec_b64 s[12:13], vcc
	s_cbranch_execz .LBB0_1651
	v_cmp_eq_f32_e32 vcc, v119, v104
	s_waitcnt lgkmcnt(0)
	v_cmp_lt_i32_e64 s[4:5], v108, v102
	s_and_b64 s[4:5], s[4:5], vcc
	s_orn2_b64 s[4:5], s[4:5], exec
